# v39 + code placement: heads of the ten GEMM K-loops aligned to 64 bytes
# baseline (speedup 1.0000x reference)
; template <int K, class Epi, class Sched, bool ALIGN_EPI>
; __device__ __forceinline__ void gemm_phase(LAS unsigned char* lds, const Gemm g, const Sched& S, const Epi& E) {
;     ...
;     f32x4 acc[2][2][4][2];
; #pragma unroll
;     for (int a = 0; a < 2; ++a)
; #pragma unroll
;         for (int b = 0; b < 2; ++b)
; #pragma unroll
;             for (int m = 0; m < 4; ++m)
; #pragma unroll
;                 for (int n = 0; n < 2; ++n) acc[a][b][m][n] = (f32x4){0.f, 0.f, 0.f, 0.f};
.LBB0_378:
	v_mov_b32_e32 v7, 0
	s_andn2_b64 vcc, exec, s[12:13]
	v_mov_b32_e32 v6, v7
	v_mov_b32_e32 v5, v7
	v_mov_b32_e32 v4, v7
	v_mov_b32_e32 v11, v7
	v_mov_b32_e32 v10, v7
	v_mov_b32_e32 v9, v7
	v_mov_b32_e32 v8, v7
	v_mov_b32_e32 v23, v7
	v_mov_b32_e32 v22, v7
	v_mov_b32_e32 v21, v7
	v_mov_b32_e32 v20, v7
	v_mov_b32_e32 v27, v7
	v_mov_b32_e32 v26, v7
	v_mov_b32_e32 v25, v7
	v_mov_b32_e32 v24, v7
	v_mov_b32_e32 v141, v7
	v_mov_b32_e32 v140, v7
	v_mov_b32_e32 v139, v7
	v_mov_b32_e32 v138, v7
	v_mov_b32_e32 v127, v7
	v_mov_b32_e32 v126, v7
	v_mov_b32_e32 v125, v7
	v_mov_b32_e32 v124, v7
	v_mov_b32_e32 v115, v7
	v_mov_b32_e32 v114, v7
	v_mov_b32_e32 v113, v7
	v_mov_b32_e32 v112, v7
	v_mov_b32_e32 v111, v7
	v_mov_b32_e32 v110, v7
	v_mov_b32_e32 v109, v7
	v_mov_b32_e32 v108, v7
	v_mov_b32_e32 v99, v7
	v_mov_b32_e32 v98, v7
	v_mov_b32_e32 v97, v7
	v_mov_b32_e32 v96, v7
	v_mov_b32_e32 v95, v7
	v_mov_b32_e32 v94, v7
	v_mov_b32_e32 v93, v7
	v_mov_b32_e32 v92, v7
	v_mov_b32_e32 v83, v7
	v_mov_b32_e32 v82, v7
	v_mov_b32_e32 v81, v7
	v_mov_b32_e32 v80, v7
	v_mov_b32_e32 v79, v7
	v_mov_b32_e32 v78, v7
	v_mov_b32_e32 v77, v7
	v_mov_b32_e32 v76, v7
	v_mov_b32_e32 v123, v7
	v_mov_b32_e32 v122, v7
	v_mov_b32_e32 v121, v7
	v_mov_b32_e32 v120, v7
	v_mov_b32_e32 v119, v7
	v_mov_b32_e32 v118, v7
	v_mov_b32_e32 v117, v7
	v_mov_b32_e32 v116, v7
	v_mov_b32_e32 v107, v7
	v_mov_b32_e32 v106, v7
	v_mov_b32_e32 v105, v7
	v_mov_b32_e32 v104, v7
	v_mov_b32_e32 v103, v7
	v_mov_b32_e32 v102, v7
	v_mov_b32_e32 v101, v7
	v_mov_b32_e32 v100, v7
	v_mov_b32_e32 v91, v7
	v_mov_b32_e32 v90, v7
	v_mov_b32_e32 v89, v7
	v_mov_b32_e32 v88, v7
	v_mov_b32_e32 v87, v7
	v_mov_b32_e32 v86, v7
	v_mov_b32_e32 v85, v7
	v_mov_b32_e32 v84, v7
	v_mov_b32_e32 v75, v7
	v_mov_b32_e32 v74, v7
	v_mov_b32_e32 v73, v7
	v_mov_b32_e32 v72, v7
	v_mov_b32_e32 v71, v7
	v_mov_b32_e32 v70, v7
	v_mov_b32_e32 v69, v7
	v_mov_b32_e32 v68, v7
	v_mov_b32_e32 v67, v7
	v_mov_b32_e32 v66, v7
	v_mov_b32_e32 v65, v7
	v_mov_b32_e32 v64, v7
	v_mov_b32_e32 v63, v7
	v_mov_b32_e32 v62, v7
	v_mov_b32_e32 v61, v7
	v_mov_b32_e32 v60, v7
	v_mov_b32_e32 v51, v7
	v_mov_b32_e32 v50, v7
	v_mov_b32_e32 v49, v7
	v_mov_b32_e32 v48, v7
	v_mov_b32_e32 v47, v7
	v_mov_b32_e32 v46, v7
	v_mov_b32_e32 v45, v7
	v_mov_b32_e32 v44, v7
	v_mov_b32_e32 v35, v7
	v_mov_b32_e32 v34, v7
	v_mov_b32_e32 v33, v7
	v_mov_b32_e32 v32, v7
	v_mov_b32_e32 v31, v7
	v_mov_b32_e32 v30, v7
	v_mov_b32_e32 v29, v7
	v_mov_b32_e32 v28, v7
	v_mov_b32_e32 v19, v7
	v_mov_b32_e32 v18, v7
	v_mov_b32_e32 v17, v7
	v_mov_b32_e32 v16, v7
	v_mov_b32_e32 v15, v7
	v_mov_b32_e32 v14, v7
	v_mov_b32_e32 v13, v7
	v_mov_b32_e32 v12, v7
	v_mov_b32_e32 v59, v7
	v_mov_b32_e32 v58, v7
	v_mov_b32_e32 v57, v7
	v_mov_b32_e32 v56, v7
	v_mov_b32_e32 v55, v7
	v_mov_b32_e32 v54, v7
	v_mov_b32_e32 v53, v7
	v_mov_b32_e32 v52, v7
	v_mov_b32_e32 v43, v7
	v_mov_b32_e32 v42, v7
	v_mov_b32_e32 v41, v7
	v_mov_b32_e32 v40, v7
	v_mov_b32_e32 v39, v7
	v_mov_b32_e32 v38, v7
	v_mov_b32_e32 v37, v7
	v_mov_b32_e32 v36, v7
	s_cbranch_vccnz .LBB0_381
	v_mov_b32_e32 v36, 0
	v_mov_b32_e32 v147, v131
	v_mov_b32_e32 v145, v131
	s_mov_b32 s33, 0
	s_mov_b64 s[26:27], 0x100
	s_mov_b64 s[66:67], s[96:97]
	v_mov_b32_e32 v37, v36
	v_mov_b32_e32 v38, v36
	v_mov_b32_e32 v39, v36
	v_mov_b32_e32 v40, v36
	v_mov_b32_e32 v41, v36
	v_mov_b32_e32 v42, v36
	v_mov_b32_e32 v43, v36
	v_mov_b32_e32 v52, v36
	v_mov_b32_e32 v53, v36
	v_mov_b32_e32 v54, v36
	v_mov_b32_e32 v55, v36
	v_mov_b32_e32 v56, v36
	v_mov_b32_e32 v57, v36
	v_mov_b32_e32 v58, v36
	v_mov_b32_e32 v59, v36
	v_mov_b32_e32 v12, v36
	v_mov_b32_e32 v13, v36
	v_mov_b32_e32 v14, v36
	v_mov_b32_e32 v15, v36
	v_mov_b32_e32 v16, v36
	v_mov_b32_e32 v17, v36
	v_mov_b32_e32 v18, v36
	v_mov_b32_e32 v19, v36
	v_mov_b32_e32 v28, v36
	v_mov_b32_e32 v29, v36
	v_mov_b32_e32 v30, v36
	v_mov_b32_e32 v31, v36
	v_mov_b32_e32 v32, v36
	v_mov_b32_e32 v33, v36
	v_mov_b32_e32 v34, v36
	v_mov_b32_e32 v35, v36
	v_mov_b32_e32 v44, v36
	v_mov_b32_e32 v45, v36
	v_mov_b32_e32 v46, v36
	v_mov_b32_e32 v47, v36
	v_mov_b32_e32 v48, v36
	v_mov_b32_e32 v49, v36
	v_mov_b32_e32 v50, v36
	v_mov_b32_e32 v51, v36
	v_mov_b32_e32 v60, v36
	v_mov_b32_e32 v61, v36
	v_mov_b32_e32 v62, v36
	v_mov_b32_e32 v63, v36
	v_mov_b32_e32 v64, v36
	v_mov_b32_e32 v65, v36
	v_mov_b32_e32 v66, v36
	v_mov_b32_e32 v67, v36
	v_mov_b32_e32 v68, v36
	v_mov_b32_e32 v69, v36
	v_mov_b32_e32 v70, v36
	v_mov_b32_e32 v71, v36
	v_mov_b32_e32 v72, v36
	v_mov_b32_e32 v73, v36
	v_mov_b32_e32 v74, v36
	v_mov_b32_e32 v75, v36
	v_mov_b32_e32 v84, v36
	v_mov_b32_e32 v85, v36
	v_mov_b32_e32 v86, v36
	v_mov_b32_e32 v87, v36
	v_mov_b32_e32 v88, v36
	v_mov_b32_e32 v89, v36
	v_mov_b32_e32 v90, v36
	v_mov_b32_e32 v91, v36
	v_mov_b32_e32 v100, v36
	v_mov_b32_e32 v101, v36
	v_mov_b32_e32 v102, v36
	v_mov_b32_e32 v103, v36
	v_mov_b32_e32 v104, v36
	v_mov_b32_e32 v105, v36
	v_mov_b32_e32 v106, v36
	v_mov_b32_e32 v107, v36
	v_mov_b32_e32 v116, v36
	v_mov_b32_e32 v117, v36
	v_mov_b32_e32 v118, v36
	v_mov_b32_e32 v119, v36
	v_mov_b32_e32 v120, v36
	v_mov_b32_e32 v121, v36
	v_mov_b32_e32 v122, v36
	v_mov_b32_e32 v123, v36
	v_mov_b32_e32 v76, v36
	v_mov_b32_e32 v77, v36
	v_mov_b32_e32 v78, v36
	v_mov_b32_e32 v79, v36
	v_mov_b32_e32 v80, v36
	v_mov_b32_e32 v81, v36
	v_mov_b32_e32 v82, v36
	v_mov_b32_e32 v83, v36
	v_mov_b32_e32 v92, v36
	v_mov_b32_e32 v93, v36
	v_mov_b32_e32 v94, v36
	v_mov_b32_e32 v95, v36
	v_mov_b32_e32 v96, v36
	v_mov_b32_e32 v97, v36
	v_mov_b32_e32 v98, v36
	v_mov_b32_e32 v99, v36
	v_mov_b32_e32 v108, v36
	v_mov_b32_e32 v109, v36
	v_mov_b32_e32 v110, v36
	v_mov_b32_e32 v111, v36
	v_mov_b32_e32 v112, v36
	v_mov_b32_e32 v113, v36
	v_mov_b32_e32 v114, v36
	v_mov_b32_e32 v115, v36
	v_mov_b32_e32 v124, v36
	v_mov_b32_e32 v125, v36
	v_mov_b32_e32 v126, v36
	v_mov_b32_e32 v127, v36
	v_mov_b32_e32 v138, v36
	v_mov_b32_e32 v139, v36
	v_mov_b32_e32 v140, v36
	v_mov_b32_e32 v141, v36
	v_mov_b32_e32 v24, v36
	v_mov_b32_e32 v25, v36
	v_mov_b32_e32 v26, v36
	v_mov_b32_e32 v27, v36
	v_mov_b32_e32 v20, v36
	v_mov_b32_e32 v21, v36
	v_mov_b32_e32 v22, v36
	v_mov_b32_e32 v23, v36
	v_mov_b32_e32 v8, v36
	v_mov_b32_e32 v9, v36
	v_mov_b32_e32 v10, v36
	v_mov_b32_e32 v11, v36
	v_mov_b32_e32 v4, v36
	v_mov_b32_e32 v5, v36
	v_mov_b32_e32 v6, v36
	v_mov_b32_e32 v7, v36
	.p2alignl 6, 3212836864

; template <int K, class Epi, class Sched, bool ALIGN_EPI>
; __device__ __forceinline__ void gemm_phase(LAS unsigned char* lds, const Gemm g, const Sched& S, const Epi& E) {
;     ...
;     f32x4 acc[2][2][4][2];
; #pragma unroll
;     for (int a = 0; a < 2; ++a)
; #pragma unroll
;         for (int b = 0; b < 2; ++b)
; #pragma unroll
;             for (int m = 0; m < 4; ++m)
; #pragma unroll
;                 for (int n = 0; n < 2; ++n) acc[a][b][m][n] = (f32x4){0.f, 0.f, 0.f, 0.f};
.LBB0_714:
	v_mov_b32_e32 v7, 0
	s_andn2_b64 vcc, exec, s[64:65]
	v_mov_b32_e32 v6, v7
	v_mov_b32_e32 v5, v7
	v_mov_b32_e32 v4, v7
	v_mov_b32_e32 v11, v7
	v_mov_b32_e32 v10, v7
	v_mov_b32_e32 v9, v7
	v_mov_b32_e32 v8, v7
	v_mov_b32_e32 v23, v7
	v_mov_b32_e32 v22, v7
	v_mov_b32_e32 v21, v7
	v_mov_b32_e32 v20, v7
	v_mov_b32_e32 v27, v7
	v_mov_b32_e32 v26, v7
	v_mov_b32_e32 v25, v7
	v_mov_b32_e32 v24, v7
	v_mov_b32_e32 v141, v7
	v_mov_b32_e32 v140, v7
	v_mov_b32_e32 v139, v7
	v_mov_b32_e32 v138, v7
	v_mov_b32_e32 v127, v7
	v_mov_b32_e32 v126, v7
	v_mov_b32_e32 v125, v7
	v_mov_b32_e32 v124, v7
	v_mov_b32_e32 v115, v7
	v_mov_b32_e32 v114, v7
	v_mov_b32_e32 v113, v7
	v_mov_b32_e32 v112, v7
	v_mov_b32_e32 v111, v7
	v_mov_b32_e32 v110, v7
	v_mov_b32_e32 v109, v7
	v_mov_b32_e32 v108, v7
	v_mov_b32_e32 v99, v7
	v_mov_b32_e32 v98, v7
	v_mov_b32_e32 v97, v7
	v_mov_b32_e32 v96, v7
	v_mov_b32_e32 v95, v7
	v_mov_b32_e32 v94, v7
	v_mov_b32_e32 v93, v7
	v_mov_b32_e32 v92, v7
	v_mov_b32_e32 v83, v7
	v_mov_b32_e32 v82, v7
	v_mov_b32_e32 v81, v7
	v_mov_b32_e32 v80, v7
	v_mov_b32_e32 v79, v7
	v_mov_b32_e32 v78, v7
	v_mov_b32_e32 v77, v7
	v_mov_b32_e32 v76, v7
	v_mov_b32_e32 v123, v7
	v_mov_b32_e32 v122, v7
	v_mov_b32_e32 v121, v7
	v_mov_b32_e32 v120, v7
	v_mov_b32_e32 v119, v7
	v_mov_b32_e32 v118, v7
	v_mov_b32_e32 v117, v7
	v_mov_b32_e32 v116, v7
	v_mov_b32_e32 v107, v7
	v_mov_b32_e32 v106, v7
	v_mov_b32_e32 v105, v7
	v_mov_b32_e32 v104, v7
	v_mov_b32_e32 v103, v7
	v_mov_b32_e32 v102, v7
	v_mov_b32_e32 v101, v7
	v_mov_b32_e32 v100, v7
	v_mov_b32_e32 v91, v7
	v_mov_b32_e32 v90, v7
	v_mov_b32_e32 v89, v7
	v_mov_b32_e32 v88, v7
	v_mov_b32_e32 v87, v7
	v_mov_b32_e32 v86, v7
	v_mov_b32_e32 v85, v7
	v_mov_b32_e32 v84, v7
	v_mov_b32_e32 v75, v7
	v_mov_b32_e32 v74, v7
	v_mov_b32_e32 v73, v7
	v_mov_b32_e32 v72, v7
	v_mov_b32_e32 v71, v7
	v_mov_b32_e32 v70, v7
	v_mov_b32_e32 v69, v7
	v_mov_b32_e32 v68, v7
	v_mov_b32_e32 v67, v7
	v_mov_b32_e32 v66, v7
	v_mov_b32_e32 v65, v7
	v_mov_b32_e32 v64, v7
	v_mov_b32_e32 v63, v7
	v_mov_b32_e32 v62, v7
	v_mov_b32_e32 v61, v7
	v_mov_b32_e32 v60, v7
	v_mov_b32_e32 v51, v7
	v_mov_b32_e32 v50, v7
	v_mov_b32_e32 v49, v7
	v_mov_b32_e32 v48, v7
	v_mov_b32_e32 v47, v7
	v_mov_b32_e32 v46, v7
	v_mov_b32_e32 v45, v7
	v_mov_b32_e32 v44, v7
	v_mov_b32_e32 v35, v7
	v_mov_b32_e32 v34, v7
	v_mov_b32_e32 v33, v7
	v_mov_b32_e32 v32, v7
	v_mov_b32_e32 v31, v7
	v_mov_b32_e32 v30, v7
	v_mov_b32_e32 v29, v7
	v_mov_b32_e32 v28, v7
	v_mov_b32_e32 v19, v7
	v_mov_b32_e32 v18, v7
	v_mov_b32_e32 v17, v7
	v_mov_b32_e32 v16, v7
	v_mov_b32_e32 v15, v7
	v_mov_b32_e32 v14, v7
	v_mov_b32_e32 v13, v7
	v_mov_b32_e32 v12, v7
	v_mov_b32_e32 v59, v7
	v_mov_b32_e32 v58, v7
	v_mov_b32_e32 v57, v7
	v_mov_b32_e32 v56, v7
	v_mov_b32_e32 v55, v7
	v_mov_b32_e32 v54, v7
	v_mov_b32_e32 v53, v7
	v_mov_b32_e32 v52, v7
	v_mov_b32_e32 v43, v7
	v_mov_b32_e32 v42, v7
	v_mov_b32_e32 v41, v7
	v_mov_b32_e32 v40, v7
	v_mov_b32_e32 v39, v7
	v_mov_b32_e32 v38, v7
	v_mov_b32_e32 v37, v7
	v_mov_b32_e32 v36, v7
	s_cbranch_vccnz .LBB0_717
	v_mov_b32_e32 v36, 0
	v_mov_b32_e32 v147, v131
	v_mov_b32_e32 v145, v131
	s_mov_b32 s42, 0
	s_mov_b64 s[76:77], 0x100
	s_mov_b64 s[78:79], s[34:35]
	v_mov_b32_e32 v37, v36
	v_mov_b32_e32 v38, v36
	v_mov_b32_e32 v39, v36
	v_mov_b32_e32 v40, v36
	v_mov_b32_e32 v41, v36
	v_mov_b32_e32 v42, v36
	v_mov_b32_e32 v43, v36
	v_mov_b32_e32 v52, v36
	v_mov_b32_e32 v53, v36
	v_mov_b32_e32 v54, v36
	v_mov_b32_e32 v55, v36
	v_mov_b32_e32 v56, v36
	v_mov_b32_e32 v57, v36
	v_mov_b32_e32 v58, v36
	v_mov_b32_e32 v59, v36
	v_mov_b32_e32 v12, v36
	v_mov_b32_e32 v13, v36
	v_mov_b32_e32 v14, v36
	v_mov_b32_e32 v15, v36
	v_mov_b32_e32 v16, v36
	v_mov_b32_e32 v17, v36
	v_mov_b32_e32 v18, v36
	v_mov_b32_e32 v19, v36
	v_mov_b32_e32 v28, v36
	v_mov_b32_e32 v29, v36
	v_mov_b32_e32 v30, v36
	v_mov_b32_e32 v31, v36
	v_mov_b32_e32 v32, v36
	v_mov_b32_e32 v33, v36
	v_mov_b32_e32 v34, v36
	v_mov_b32_e32 v35, v36
	v_mov_b32_e32 v44, v36
	v_mov_b32_e32 v45, v36
	v_mov_b32_e32 v46, v36
	v_mov_b32_e32 v47, v36
	v_mov_b32_e32 v48, v36
	v_mov_b32_e32 v49, v36
	v_mov_b32_e32 v50, v36
	v_mov_b32_e32 v51, v36
	v_mov_b32_e32 v60, v36
	v_mov_b32_e32 v61, v36
	v_mov_b32_e32 v62, v36
	v_mov_b32_e32 v63, v36
	v_mov_b32_e32 v64, v36
	v_mov_b32_e32 v65, v36
	v_mov_b32_e32 v66, v36
	v_mov_b32_e32 v67, v36
	v_mov_b32_e32 v68, v36
	v_mov_b32_e32 v69, v36
	v_mov_b32_e32 v70, v36
	v_mov_b32_e32 v71, v36
	v_mov_b32_e32 v72, v36
	v_mov_b32_e32 v73, v36
	v_mov_b32_e32 v74, v36
	v_mov_b32_e32 v75, v36
	v_mov_b32_e32 v84, v36
	v_mov_b32_e32 v85, v36
	v_mov_b32_e32 v86, v36
	v_mov_b32_e32 v87, v36
	v_mov_b32_e32 v88, v36
	v_mov_b32_e32 v89, v36
	v_mov_b32_e32 v90, v36
	v_mov_b32_e32 v91, v36
	v_mov_b32_e32 v100, v36
	v_mov_b32_e32 v101, v36
	v_mov_b32_e32 v102, v36
	v_mov_b32_e32 v103, v36
	v_mov_b32_e32 v104, v36
	v_mov_b32_e32 v105, v36
	v_mov_b32_e32 v106, v36
	v_mov_b32_e32 v107, v36
	v_mov_b32_e32 v116, v36
	v_mov_b32_e32 v117, v36
	v_mov_b32_e32 v118, v36
	v_mov_b32_e32 v119, v36
	v_mov_b32_e32 v120, v36
	v_mov_b32_e32 v121, v36
	v_mov_b32_e32 v122, v36
	v_mov_b32_e32 v123, v36
	v_mov_b32_e32 v76, v36
	v_mov_b32_e32 v77, v36
	v_mov_b32_e32 v78, v36
	v_mov_b32_e32 v79, v36
	v_mov_b32_e32 v80, v36
	v_mov_b32_e32 v81, v36
	v_mov_b32_e32 v82, v36
	v_mov_b32_e32 v83, v36
	v_mov_b32_e32 v92, v36
	v_mov_b32_e32 v93, v36
	v_mov_b32_e32 v94, v36
	v_mov_b32_e32 v95, v36
	v_mov_b32_e32 v96, v36
	v_mov_b32_e32 v97, v36
	v_mov_b32_e32 v98, v36
	v_mov_b32_e32 v99, v36
	v_mov_b32_e32 v108, v36
	v_mov_b32_e32 v109, v36
	v_mov_b32_e32 v110, v36
	v_mov_b32_e32 v111, v36
	v_mov_b32_e32 v112, v36
	v_mov_b32_e32 v113, v36
	v_mov_b32_e32 v114, v36
	v_mov_b32_e32 v115, v36
	v_mov_b32_e32 v124, v36
	v_mov_b32_e32 v125, v36
	v_mov_b32_e32 v126, v36
	v_mov_b32_e32 v127, v36
	v_mov_b32_e32 v138, v36
	v_mov_b32_e32 v139, v36
	v_mov_b32_e32 v140, v36
	v_mov_b32_e32 v141, v36
	v_mov_b32_e32 v24, v36
	v_mov_b32_e32 v25, v36
	v_mov_b32_e32 v26, v36
	v_mov_b32_e32 v27, v36
	v_mov_b32_e32 v20, v36
	v_mov_b32_e32 v21, v36
	v_mov_b32_e32 v22, v36
	v_mov_b32_e32 v23, v36
	v_mov_b32_e32 v8, v36
	v_mov_b32_e32 v9, v36
	v_mov_b32_e32 v10, v36
	v_mov_b32_e32 v11, v36
	v_mov_b32_e32 v4, v36
	v_mov_b32_e32 v5, v36
	v_mov_b32_e32 v6, v36
	v_mov_b32_e32 v7, v36
	.p2alignl 6, 3212836864

; template <int K, class Epi, class Sched, bool ALIGN_EPI>
; __device__ __forceinline__ void gemm_phase(LAS unsigned char* lds, const Gemm g, const Sched& S, const Epi& E) {
;     ...
;     f32x4 acc[2][2][4][2];
; #pragma unroll
;     for (int a = 0; a < 2; ++a)
; #pragma unroll
;         for (int b = 0; b < 2; ++b)
; #pragma unroll
;             for (int m = 0; m < 4; ++m)
; #pragma unroll
;                 for (int n = 0; n < 2; ++n) acc[a][b][m][n] = (f32x4){0.f, 0.f, 0.f, 0.f};
;     ...
;             if constexpr (Epi::HAS_MID) { if (t == nt / 2) E.mid(acc, cur, wr, wc, fr, fq, tab0 + (ui & 1) * 256); }
.LBB0_1618:
	v_mov_b32_e32 v7, 0
	s_andn2_b64 vcc, exec, s[34:35]
	v_mov_b32_e32 v6, 0
	v_mov_b32_e32 v5, 0
	v_mov_b32_e32 v4, 0
	v_mov_b32_e32 v11, 0
	v_mov_b32_e32 v10, 0
	v_mov_b32_e32 v9, 0
	v_mov_b32_e32 v8, 0
	v_mov_b32_e32 v23, 0
	v_mov_b32_e32 v22, 0
	v_mov_b32_e32 v21, 0
	v_mov_b32_e32 v20, 0
	v_mov_b32_e32 v27, 0
	v_mov_b32_e32 v26, 0
	v_mov_b32_e32 v25, 0
	v_mov_b32_e32 v24, 0
	v_mov_b32_e32 v119, 0
	v_mov_b32_e32 v118, 0
	v_mov_b32_e32 v117, 0
	v_mov_b32_e32 v116, 0
	v_mov_b32_e32 v123, 0
	v_mov_b32_e32 v122, 0
	v_mov_b32_e32 v121, 0
	v_mov_b32_e32 v120, 0
	v_mov_b32_e32 v115, 0
	v_mov_b32_e32 v114, 0
	v_mov_b32_e32 v113, 0
	v_mov_b32_e32 v112, 0
	v_mov_b32_e32 v111, 0
	v_mov_b32_e32 v110, 0
	v_mov_b32_e32 v109, 0
	v_mov_b32_e32 v108, 0
	v_mov_b32_e32 v99, 0
	v_mov_b32_e32 v98, 0
	v_mov_b32_e32 v97, 0
	v_mov_b32_e32 v96, 0
	v_mov_b32_e32 v95, 0
	v_mov_b32_e32 v94, 0
	v_mov_b32_e32 v93, 0
	v_mov_b32_e32 v92, 0
	v_mov_b32_e32 v83, 0
	v_mov_b32_e32 v82, 0
	v_mov_b32_e32 v81, 0
	v_mov_b32_e32 v80, 0
	v_mov_b32_e32 v79, 0
	v_mov_b32_e32 v78, 0
	v_mov_b32_e32 v77, 0
	v_mov_b32_e32 v76, 0
	v_mov_b32_e32 v141, 0
	v_mov_b32_e32 v140, 0
	v_mov_b32_e32 v139, 0
	v_mov_b32_e32 v138, 0
	v_mov_b32_e32 v127, 0
	v_mov_b32_e32 v126, 0
	v_mov_b32_e32 v125, 0
	v_mov_b32_e32 v124, 0
	v_mov_b32_e32 v107, 0
	v_mov_b32_e32 v106, 0
	v_mov_b32_e32 v105, 0
	v_mov_b32_e32 v104, 0
	v_mov_b32_e32 v103, 0
	v_mov_b32_e32 v102, 0
	v_mov_b32_e32 v101, 0
	v_mov_b32_e32 v100, 0
	v_mov_b32_e32 v91, 0
	v_mov_b32_e32 v90, 0
	v_mov_b32_e32 v89, 0
	v_mov_b32_e32 v88, 0
	v_mov_b32_e32 v87, 0
	v_mov_b32_e32 v86, 0
	v_mov_b32_e32 v85, 0
	v_mov_b32_e32 v84, 0
	v_mov_b32_e32 v75, 0
	v_mov_b32_e32 v74, 0
	v_mov_b32_e32 v73, 0
	v_mov_b32_e32 v72, 0
	v_mov_b32_e32 v71, 0
	v_mov_b32_e32 v70, 0
	v_mov_b32_e32 v69, 0
	v_mov_b32_e32 v68, 0
	v_mov_b32_e32 v63, 0
	v_mov_b32_e32 v62, 0
	v_mov_b32_e32 v61, 0
	v_mov_b32_e32 v60, 0
	v_mov_b32_e32 v67, 0
	v_mov_b32_e32 v66, 0
	v_mov_b32_e32 v65, 0
	v_mov_b32_e32 v64, 0
	v_mov_b32_e32 v51, 0
	v_mov_b32_e32 v50, 0
	v_mov_b32_e32 v49, 0
	v_mov_b32_e32 v48, 0
	v_mov_b32_e32 v47, 0
	v_mov_b32_e32 v46, 0
	v_mov_b32_e32 v45, 0
	v_mov_b32_e32 v44, 0
	v_mov_b32_e32 v35, 0
	v_mov_b32_e32 v34, 0
	v_mov_b32_e32 v33, 0
	v_mov_b32_e32 v32, 0
	v_mov_b32_e32 v31, 0
	v_mov_b32_e32 v30, 0
	v_mov_b32_e32 v29, 0
	v_mov_b32_e32 v28, 0
	v_mov_b32_e32 v19, 0
	v_mov_b32_e32 v18, 0
	v_mov_b32_e32 v17, 0
	v_mov_b32_e32 v16, 0
	v_mov_b32_e32 v15, 0
	v_mov_b32_e32 v14, 0
	v_mov_b32_e32 v13, 0
	v_mov_b32_e32 v12, 0
	v_mov_b32_e32 v59, 0
	v_mov_b32_e32 v58, 0
	v_mov_b32_e32 v57, 0
	v_mov_b32_e32 v56, 0
	v_mov_b32_e32 v55, 0
	v_mov_b32_e32 v54, 0
	v_mov_b32_e32 v53, 0
	v_mov_b32_e32 v52, 0
	v_mov_b32_e32 v43, 0
	v_mov_b32_e32 v42, 0
	v_mov_b32_e32 v41, 0
	v_mov_b32_e32 v40, 0
	v_mov_b32_e32 v39, 0
	v_mov_b32_e32 v38, 0
	v_mov_b32_e32 v37, 0
	v_mov_b32_e32 v36, 0
	s_cbranch_vccnz .LBB0_1623
	s_lshl_b32 s42, s85, 11
	v_mov_b32_e32 v130, v131
	v_mov_b32_e32 v132, v131
	v_mov_b32_e32 v133, v131
	s_and_b32 s42, s42, 0x800
	v_mov_b32_e32 v145, v131
	v_mov_b32_e32 v147, v131
	v_mov_b64_e32 v[36:37], v[130:131]
	v_mov_b64_e32 v[40:41], v[130:131]
	v_mov_b64_e32 v[52:53], v[130:131]
	v_mov_b64_e32 v[56:57], v[130:131]
	v_mov_b64_e32 v[12:13], v[130:131]
	v_mov_b64_e32 v[16:17], v[130:131]
	v_mov_b64_e32 v[28:29], v[130:131]
	v_mov_b64_e32 v[32:33], v[130:131]
	v_mov_b64_e32 v[44:45], v[130:131]
	v_mov_b64_e32 v[48:49], v[130:131]
	v_mov_b64_e32 v[64:65], v[130:131]
	v_mov_b64_e32 v[60:61], v[130:131]
	v_mov_b64_e32 v[68:69], v[130:131]
	v_mov_b64_e32 v[72:73], v[130:131]
	v_mov_b64_e32 v[84:85], v[130:131]
	v_mov_b64_e32 v[88:89], v[130:131]
	v_mov_b64_e32 v[100:101], v[130:131]
	v_mov_b64_e32 v[104:105], v[130:131]
	v_mov_b64_e32 v[124:125], v[130:131]
	v_mov_b64_e32 v[140:141], v[132:133]
	v_mov_b64_e32 v[76:77], v[130:131]
	v_mov_b64_e32 v[80:81], v[130:131]
	v_mov_b64_e32 v[92:93], v[130:131]
	v_mov_b64_e32 v[96:97], v[130:131]
	v_mov_b64_e32 v[108:109], v[130:131]
	v_mov_b64_e32 v[112:113], v[130:131]
	v_mov_b64_e32 v[120:121], v[130:131]
	v_mov_b64_e32 v[116:117], v[130:131]
	v_mov_b64_e32 v[24:25], v[130:131]
	v_mov_b64_e32 v[20:21], v[130:131]
	v_mov_b64_e32 v[8:9], v[130:131]
	v_mov_b64_e32 v[4:5], v[130:131]
	v_add_u32_e32 v143, s42, v186
	v_lshl_add_u64 v[150:151], s[50:51], 0, v[144:145]
	v_lshl_add_u64 v[152:153], s[50:51], 0, v[146:147]
	s_mov_b32 s86, 0
	s_mov_b64 s[42:43], 0x100
	v_mov_b64_e32 v[38:39], v[132:133]
	v_mov_b64_e32 v[42:43], v[132:133]
	v_mov_b64_e32 v[54:55], v[132:133]
	v_mov_b64_e32 v[58:59], v[132:133]
	v_mov_b64_e32 v[14:15], v[132:133]
	v_mov_b64_e32 v[18:19], v[132:133]
	v_mov_b64_e32 v[30:31], v[132:133]
	v_mov_b64_e32 v[34:35], v[132:133]
	v_mov_b64_e32 v[46:47], v[132:133]
	v_mov_b64_e32 v[50:51], v[132:133]
	v_mov_b64_e32 v[66:67], v[132:133]
	v_mov_b64_e32 v[62:63], v[132:133]
	v_mov_b64_e32 v[70:71], v[132:133]
	v_mov_b64_e32 v[74:75], v[132:133]
	v_mov_b64_e32 v[86:87], v[132:133]
	v_mov_b64_e32 v[90:91], v[132:133]
	v_mov_b64_e32 v[102:103], v[132:133]
	v_mov_b64_e32 v[106:107], v[132:133]
	v_mov_b64_e32 v[126:127], v[132:133]
	v_mov_b64_e32 v[138:139], v[130:131]
	v_mov_b64_e32 v[78:79], v[132:133]
	v_mov_b64_e32 v[82:83], v[132:133]
	v_mov_b64_e32 v[94:95], v[132:133]
	v_mov_b64_e32 v[98:99], v[132:133]
	v_mov_b64_e32 v[110:111], v[132:133]
	v_mov_b64_e32 v[114:115], v[132:133]
	v_mov_b64_e32 v[122:123], v[132:133]
	v_mov_b64_e32 v[118:119], v[132:133]
	v_mov_b64_e32 v[26:27], v[132:133]
	v_mov_b64_e32 v[22:23], v[132:133]
	v_mov_b64_e32 v[10:11], v[132:133]
	v_mov_b64_e32 v[6:7], v[132:133]
	s_branch .LBB0_1621
	.p2alignl 6, 3212836864

; template <int K, class Epi, class Sched, bool ALIGN_EPI>
; __device__ __forceinline__ void gemm_phase(LAS unsigned char* lds, const Gemm g, const Sched& S, const Epi& E) {
;     ...
;     f32x4 acc[2][2][4][2];
; #pragma unroll
;     for (int a = 0; a < 2; ++a)
; #pragma unroll
;         for (int b = 0; b < 2; ++b)
; #pragma unroll
;             for (int m = 0; m < 4; ++m)
; #pragma unroll
;                 for (int n = 0; n < 2; ++n) acc[a][b][m][n] = (f32x4){0.f, 0.f, 0.f, 0.f};
.LBB0_1722:
	v_mov_b32_e32 v15, 0
	s_andn2_b64 vcc, exec, s[58:59]
	v_mov_b32_e32 v14, v15
	v_mov_b32_e32 v13, v15
	s_waitcnt lgkmcnt(0)
	v_mov_b32_e32 v12, v15
	v_mov_b32_e32 v27, v15
	v_mov_b32_e32 v26, v15
	v_mov_b32_e32 v25, v15
	v_mov_b32_e32 v24, v15
	s_waitcnt vmcnt(0)
	v_mov_b32_e32 v95, v15
	v_mov_b32_e32 v94, v15
	v_mov_b32_e32 v93, v15
	v_mov_b32_e32 v92, v15
	v_mov_b32_e32 v91, v15
	v_mov_b32_e32 v90, v15
	v_mov_b32_e32 v89, v15
	v_mov_b32_e32 v88, v15
	v_mov_b32_e32 v83, v15
	v_mov_b32_e32 v82, v15
	v_mov_b32_e32 v81, v15
	v_mov_b32_e32 v80, v15
	v_mov_b32_e32 v79, v15
	v_mov_b32_e32 v78, v15
	v_mov_b32_e32 v77, v15
	v_mov_b32_e32 v76, v15
	v_mov_b32_e32 v71, v15
	v_mov_b32_e32 v70, v15
	v_mov_b32_e32 v69, v15
	v_mov_b32_e32 v68, v15
	v_mov_b32_e32 v67, v15
	v_mov_b32_e32 v66, v15
	v_mov_b32_e32 v65, v15
	v_mov_b32_e32 v64, v15
	v_mov_b32_e32 v59, v15
	v_mov_b32_e32 v58, v15
	v_mov_b32_e32 v57, v15
	v_mov_b32_e32 v56, v15
	v_mov_b32_e32 v55, v15
	v_mov_b32_e32 v54, v15
	v_mov_b32_e32 v53, v15
	v_mov_b32_e32 v52, v15
	v_mov_b32_e32 v99, v15
	v_mov_b32_e32 v98, v15
	v_mov_b32_e32 v97, v15
	v_mov_b32_e32 v96, v15
	v_mov_b32_e32 v87, v15
	v_mov_b32_e32 v86, v15
	v_mov_b32_e32 v85, v15
	v_mov_b32_e32 v84, v15
	v_mov_b32_e32 v75, v15
	v_mov_b32_e32 v74, v15
	v_mov_b32_e32 v73, v15
	v_mov_b32_e32 v72, v15
	v_mov_b32_e32 v63, v15
	v_mov_b32_e32 v62, v15
	v_mov_b32_e32 v61, v15
	v_mov_b32_e32 v60, v15
	v_mov_b32_e32 v47, v15
	v_mov_b32_e32 v46, v15
	v_mov_b32_e32 v45, v15
	v_mov_b32_e32 v44, v15
	v_mov_b32_e32 v43, v15
	v_mov_b32_e32 v42, v15
	v_mov_b32_e32 v41, v15
	v_mov_b32_e32 v40, v15
	v_mov_b32_e32 v35, v15
	v_mov_b32_e32 v34, v15
	v_mov_b32_e32 v33, v15
	v_mov_b32_e32 v32, v15
	v_mov_b32_e32 v31, v15
	v_mov_b32_e32 v30, v15
	v_mov_b32_e32 v29, v15
	v_mov_b32_e32 v28, v15
	v_mov_b32_e32 v23, v15
	v_mov_b32_e32 v22, v15
	v_mov_b32_e32 v21, v15
	v_mov_b32_e32 v20, v15
	v_mov_b32_e32 v19, v15
	v_mov_b32_e32 v18, v15
	v_mov_b32_e32 v17, v15
	v_mov_b32_e32 v16, v15
	v_mov_b32_e32 v11, v15
	v_mov_b32_e32 v10, v15
	v_mov_b32_e32 v9, v15
	v_mov_b32_e32 v8, v15
	v_mov_b32_e32 v7, v15
	v_mov_b32_e32 v6, v15
	v_mov_b32_e32 v5, v15
	v_mov_b32_e32 v4, v15
	v_mov_b32_e32 v51, v15
	v_mov_b32_e32 v50, v15
	v_mov_b32_e32 v49, v15
	v_mov_b32_e32 v48, v15
	v_mov_b32_e32 v39, v15
	v_mov_b32_e32 v38, v15
	v_mov_b32_e32 v37, v15
	v_mov_b32_e32 v36, v15
	s_cbranch_vccnz .LBB0_1725
	v_mov_b32_e32 v36, 0
	v_mov_b32_e32 v109, v131
	v_mov_b32_e32 v107, v131
	s_mov_b32 s47, 0
	s_mov_b64 s[28:29], 0x100
	s_mov_b64 s[34:35], s[44:45]
	v_mov_b32_e32 v37, v36
	v_mov_b32_e32 v38, v36
	v_mov_b32_e32 v39, v36
	v_mov_b32_e32 v48, v36
	v_mov_b32_e32 v49, v36
	v_mov_b32_e32 v50, v36
	v_mov_b32_e32 v51, v36
	v_mov_b32_e32 v4, v36
	v_mov_b32_e32 v5, v36
	v_mov_b32_e32 v6, v36
	v_mov_b32_e32 v7, v36
	v_mov_b32_e32 v8, v36
	v_mov_b32_e32 v9, v36
	v_mov_b32_e32 v10, v36
	v_mov_b32_e32 v11, v36
	v_mov_b32_e32 v16, v36
	v_mov_b32_e32 v17, v36
	v_mov_b32_e32 v18, v36
	v_mov_b32_e32 v19, v36
	v_mov_b32_e32 v20, v36
	v_mov_b32_e32 v21, v36
	v_mov_b32_e32 v22, v36
	v_mov_b32_e32 v23, v36
	v_mov_b32_e32 v28, v36
	v_mov_b32_e32 v29, v36
	v_mov_b32_e32 v30, v36
	v_mov_b32_e32 v31, v36
	v_mov_b32_e32 v32, v36
	v_mov_b32_e32 v33, v36
	v_mov_b32_e32 v34, v36
	v_mov_b32_e32 v35, v36
	v_mov_b32_e32 v40, v36
	v_mov_b32_e32 v41, v36
	v_mov_b32_e32 v42, v36
	v_mov_b32_e32 v43, v36
	v_mov_b32_e32 v44, v36
	v_mov_b32_e32 v45, v36
	v_mov_b32_e32 v46, v36
	v_mov_b32_e32 v47, v36
	v_mov_b32_e32 v60, v36
	v_mov_b32_e32 v61, v36
	v_mov_b32_e32 v62, v36
	v_mov_b32_e32 v63, v36
	v_mov_b32_e32 v72, v36
	v_mov_b32_e32 v73, v36
	v_mov_b32_e32 v74, v36
	v_mov_b32_e32 v75, v36
	v_mov_b32_e32 v84, v36
	v_mov_b32_e32 v85, v36
	v_mov_b32_e32 v86, v36
	v_mov_b32_e32 v87, v36
	v_mov_b32_e32 v96, v36
	v_mov_b32_e32 v97, v36
	v_mov_b32_e32 v98, v36
	v_mov_b32_e32 v99, v36
	v_mov_b32_e32 v52, v36
	v_mov_b32_e32 v53, v36
	v_mov_b32_e32 v54, v36
	v_mov_b32_e32 v55, v36
	v_mov_b32_e32 v56, v36
	v_mov_b32_e32 v57, v36
	v_mov_b32_e32 v58, v36
	v_mov_b32_e32 v59, v36
	v_mov_b32_e32 v64, v36
	v_mov_b32_e32 v65, v36
	v_mov_b32_e32 v66, v36
	v_mov_b32_e32 v67, v36
	v_mov_b32_e32 v68, v36
	v_mov_b32_e32 v69, v36
	v_mov_b32_e32 v70, v36
	v_mov_b32_e32 v71, v36
	v_mov_b32_e32 v76, v36
	v_mov_b32_e32 v77, v36
	v_mov_b32_e32 v78, v36
	v_mov_b32_e32 v79, v36
	v_mov_b32_e32 v80, v36
	v_mov_b32_e32 v81, v36
	v_mov_b32_e32 v82, v36
	v_mov_b32_e32 v83, v36
	v_mov_b32_e32 v88, v36
	v_mov_b32_e32 v89, v36
	v_mov_b32_e32 v90, v36
	v_mov_b32_e32 v91, v36
	v_mov_b32_e32 v92, v36
	v_mov_b32_e32 v93, v36
	v_mov_b32_e32 v94, v36
	v_mov_b32_e32 v95, v36
	v_mov_b32_e32 v24, v36
	v_mov_b32_e32 v25, v36
	v_mov_b32_e32 v26, v36
	v_mov_b32_e32 v27, v36
	v_mov_b32_e32 v12, v36
	v_mov_b32_e32 v13, v36
	v_mov_b32_e32 v14, v36
	v_mov_b32_e32 v15, v36
	.p2alignl 6, 3212836864

; template <int K, class Epi, class Sched, bool ALIGN_EPI>
; __device__ __forceinline__ void gemm_phase(LAS unsigned char* lds, const Gemm g, const Sched& S, const Epi& E) {
;     ...
;     f32x4 acc[2][2][4][2];
; #pragma unroll
;     for (int a = 0; a < 2; ++a)
; #pragma unroll
;         for (int b = 0; b < 2; ++b)
; #pragma unroll
;             for (int m = 0; m < 4; ++m)
; #pragma unroll
;                 for (int n = 0; n < 2; ++n) acc[a][b][m][n] = (f32x4){0.f, 0.f, 0.f, 0.f};
.LBB0_1797:
	v_mov_b32_e32 v7, 0
	s_andn2_b64 vcc, exec, s[28:29]
	v_mov_b32_e32 v6, v7
	v_mov_b32_e32 v5, v7
	v_mov_b32_e32 v4, v7
	v_mov_b32_e32 v11, v7
	v_mov_b32_e32 v10, v7
	v_mov_b32_e32 v9, v7
	v_mov_b32_e32 v8, v7
	v_mov_b32_e32 v23, v7
	v_mov_b32_e32 v22, v7
	v_mov_b32_e32 v21, v7
	v_mov_b32_e32 v20, v7
	v_mov_b32_e32 v27, v7
	v_mov_b32_e32 v26, v7
	v_mov_b32_e32 v25, v7
	v_mov_b32_e32 v24, v7
	v_mov_b32_e32 v141, v7
	v_mov_b32_e32 v140, v7
	v_mov_b32_e32 v139, v7
	v_mov_b32_e32 v138, v7
	v_mov_b32_e32 v127, v7
	v_mov_b32_e32 v126, v7
	v_mov_b32_e32 v125, v7
	v_mov_b32_e32 v124, v7
	v_mov_b32_e32 v115, v7
	v_mov_b32_e32 v114, v7
	v_mov_b32_e32 v113, v7
	v_mov_b32_e32 v112, v7
	v_mov_b32_e32 v111, v7
	v_mov_b32_e32 v110, v7
	v_mov_b32_e32 v109, v7
	v_mov_b32_e32 v108, v7
	v_mov_b32_e32 v99, v7
	v_mov_b32_e32 v98, v7
	v_mov_b32_e32 v97, v7
	v_mov_b32_e32 v96, v7
	v_mov_b32_e32 v95, v7
	v_mov_b32_e32 v94, v7
	v_mov_b32_e32 v93, v7
	v_mov_b32_e32 v92, v7
	v_mov_b32_e32 v83, v7
	v_mov_b32_e32 v82, v7
	v_mov_b32_e32 v81, v7
	v_mov_b32_e32 v80, v7
	v_mov_b32_e32 v79, v7
	v_mov_b32_e32 v78, v7
	v_mov_b32_e32 v77, v7
	v_mov_b32_e32 v76, v7
	v_mov_b32_e32 v123, v7
	v_mov_b32_e32 v122, v7
	v_mov_b32_e32 v121, v7
	v_mov_b32_e32 v120, v7
	v_mov_b32_e32 v119, v7
	v_mov_b32_e32 v118, v7
	v_mov_b32_e32 v117, v7
	v_mov_b32_e32 v116, v7
	v_mov_b32_e32 v107, v7
	v_mov_b32_e32 v106, v7
	v_mov_b32_e32 v105, v7
	v_mov_b32_e32 v104, v7
	v_mov_b32_e32 v103, v7
	v_mov_b32_e32 v102, v7
	v_mov_b32_e32 v101, v7
	v_mov_b32_e32 v100, v7
	v_mov_b32_e32 v91, v7
	v_mov_b32_e32 v90, v7
	v_mov_b32_e32 v89, v7
	v_mov_b32_e32 v88, v7
	v_mov_b32_e32 v87, v7
	v_mov_b32_e32 v86, v7
	v_mov_b32_e32 v85, v7
	v_mov_b32_e32 v84, v7
	v_mov_b32_e32 v75, v7
	v_mov_b32_e32 v74, v7
	v_mov_b32_e32 v73, v7
	v_mov_b32_e32 v72, v7
	v_mov_b32_e32 v71, v7
	v_mov_b32_e32 v70, v7
	v_mov_b32_e32 v69, v7
	v_mov_b32_e32 v68, v7
	v_mov_b32_e32 v67, v7
	v_mov_b32_e32 v66, v7
	v_mov_b32_e32 v65, v7
	v_mov_b32_e32 v64, v7
	v_mov_b32_e32 v63, v7
	v_mov_b32_e32 v62, v7
	v_mov_b32_e32 v61, v7
	v_mov_b32_e32 v60, v7
	v_mov_b32_e32 v51, v7
	v_mov_b32_e32 v50, v7
	v_mov_b32_e32 v49, v7
	v_mov_b32_e32 v48, v7
	v_mov_b32_e32 v47, v7
	v_mov_b32_e32 v46, v7
	v_mov_b32_e32 v45, v7
	v_mov_b32_e32 v44, v7
	v_mov_b32_e32 v35, v7
	v_mov_b32_e32 v34, v7
	v_mov_b32_e32 v33, v7
	v_mov_b32_e32 v32, v7
	v_mov_b32_e32 v31, v7
	v_mov_b32_e32 v30, v7
	v_mov_b32_e32 v29, v7
	v_mov_b32_e32 v28, v7
	v_mov_b32_e32 v19, v7
	v_mov_b32_e32 v18, v7
	v_mov_b32_e32 v17, v7
	v_mov_b32_e32 v16, v7
	v_mov_b32_e32 v15, v7
	v_mov_b32_e32 v14, v7
	v_mov_b32_e32 v13, v7
	v_mov_b32_e32 v12, v7
	v_mov_b32_e32 v59, v7
	v_mov_b32_e32 v58, v7
	v_mov_b32_e32 v57, v7
	v_mov_b32_e32 v56, v7
	v_mov_b32_e32 v55, v7
	v_mov_b32_e32 v54, v7
	v_mov_b32_e32 v53, v7
	v_mov_b32_e32 v52, v7
	v_mov_b32_e32 v43, v7
	v_mov_b32_e32 v42, v7
	v_mov_b32_e32 v41, v7
	v_mov_b32_e32 v40, v7
	v_mov_b32_e32 v39, v7
	v_mov_b32_e32 v38, v7
	v_mov_b32_e32 v37, v7
	v_mov_b32_e32 v36, v7
	s_cbranch_vccnz .LBB0_1800
	v_mov_b32_e32 v145, v131
	v_mov_b32_e32 v147, v131
	s_add_u32 s75, s36, 0x100
	v_mov_b32_e32 v36, 0
	s_addc_u32 s76, s37, 0
	v_lshl_add_u64 v[150:151], s[0:1], 0, v[144:145]
	v_lshl_add_u64 v[152:153], s[0:1], 0, v[146:147]
	s_mov_b32 s77, 0
	s_mov_b64 s[36:37], 0
	v_mov_b32_e32 v37, v36
	v_mov_b32_e32 v38, v36
	v_mov_b32_e32 v39, v36
	v_mov_b32_e32 v40, v36
	v_mov_b32_e32 v41, v36
	v_mov_b32_e32 v42, v36
	v_mov_b32_e32 v43, v36
	v_mov_b32_e32 v52, v36
	v_mov_b32_e32 v53, v36
	v_mov_b32_e32 v54, v36
	v_mov_b32_e32 v55, v36
	v_mov_b32_e32 v56, v36
	v_mov_b32_e32 v57, v36
	v_mov_b32_e32 v58, v36
	v_mov_b32_e32 v59, v36
	v_mov_b32_e32 v12, v36
	v_mov_b32_e32 v13, v36
	v_mov_b32_e32 v14, v36
	v_mov_b32_e32 v15, v36
	v_mov_b32_e32 v16, v36
	v_mov_b32_e32 v17, v36
	v_mov_b32_e32 v18, v36
	v_mov_b32_e32 v19, v36
	v_mov_b32_e32 v28, v36
	v_mov_b32_e32 v29, v36
	v_mov_b32_e32 v30, v36
	v_mov_b32_e32 v31, v36
	v_mov_b32_e32 v32, v36
	v_mov_b32_e32 v33, v36
	v_mov_b32_e32 v34, v36
	v_mov_b32_e32 v35, v36
	v_mov_b32_e32 v44, v36
	v_mov_b32_e32 v45, v36
	v_mov_b32_e32 v46, v36
	v_mov_b32_e32 v47, v36
	v_mov_b32_e32 v48, v36
	v_mov_b32_e32 v49, v36
	v_mov_b32_e32 v50, v36
	v_mov_b32_e32 v51, v36
	v_mov_b32_e32 v60, v36
	v_mov_b32_e32 v61, v36
	v_mov_b32_e32 v62, v36
	v_mov_b32_e32 v63, v36
	v_mov_b32_e32 v64, v36
	v_mov_b32_e32 v65, v36
	v_mov_b32_e32 v66, v36
	v_mov_b32_e32 v67, v36
	v_mov_b32_e32 v68, v36
	v_mov_b32_e32 v69, v36
	v_mov_b32_e32 v70, v36
	v_mov_b32_e32 v71, v36
	v_mov_b32_e32 v72, v36
	v_mov_b32_e32 v73, v36
	v_mov_b32_e32 v74, v36
	v_mov_b32_e32 v75, v36
	v_mov_b32_e32 v84, v36
	v_mov_b32_e32 v85, v36
	v_mov_b32_e32 v86, v36
	v_mov_b32_e32 v87, v36
	v_mov_b32_e32 v88, v36
	v_mov_b32_e32 v89, v36
	v_mov_b32_e32 v90, v36
	v_mov_b32_e32 v91, v36
	v_mov_b32_e32 v100, v36
	v_mov_b32_e32 v101, v36
	v_mov_b32_e32 v102, v36
	v_mov_b32_e32 v103, v36
	v_mov_b32_e32 v104, v36
	v_mov_b32_e32 v105, v36
	v_mov_b32_e32 v106, v36
	v_mov_b32_e32 v107, v36
	v_mov_b32_e32 v116, v36
	v_mov_b32_e32 v117, v36
	v_mov_b32_e32 v118, v36
	v_mov_b32_e32 v119, v36
	v_mov_b32_e32 v120, v36
	v_mov_b32_e32 v121, v36
	v_mov_b32_e32 v122, v36
	v_mov_b32_e32 v123, v36
	v_mov_b32_e32 v76, v36
	v_mov_b32_e32 v77, v36
	v_mov_b32_e32 v78, v36
	v_mov_b32_e32 v79, v36
	v_mov_b32_e32 v80, v36
	v_mov_b32_e32 v81, v36
	v_mov_b32_e32 v82, v36
	v_mov_b32_e32 v83, v36
	v_mov_b32_e32 v92, v36
	v_mov_b32_e32 v93, v36
	v_mov_b32_e32 v94, v36
	v_mov_b32_e32 v95, v36
	v_mov_b32_e32 v96, v36
	v_mov_b32_e32 v97, v36
	v_mov_b32_e32 v98, v36
	v_mov_b32_e32 v99, v36
	v_mov_b32_e32 v108, v36
	v_mov_b32_e32 v109, v36
	v_mov_b32_e32 v110, v36
	v_mov_b32_e32 v111, v36
	v_mov_b32_e32 v112, v36
	v_mov_b32_e32 v113, v36
	v_mov_b32_e32 v114, v36
	v_mov_b32_e32 v115, v36
	v_mov_b32_e32 v124, v36
	v_mov_b32_e32 v125, v36
	v_mov_b32_e32 v126, v36
	v_mov_b32_e32 v127, v36
	v_mov_b32_e32 v138, v36
	v_mov_b32_e32 v139, v36
	v_mov_b32_e32 v140, v36
	v_mov_b32_e32 v141, v36
	v_mov_b32_e32 v24, v36
	v_mov_b32_e32 v25, v36
	v_mov_b32_e32 v26, v36
	v_mov_b32_e32 v27, v36
	v_mov_b32_e32 v20, v36
	v_mov_b32_e32 v21, v36
	v_mov_b32_e32 v22, v36
	v_mov_b32_e32 v23, v36
	v_mov_b32_e32 v8, v36
	v_mov_b32_e32 v9, v36
	v_mov_b32_e32 v10, v36
	v_mov_b32_e32 v11, v36
	v_mov_b32_e32 v4, v36
	v_mov_b32_e32 v5, v36
	v_mov_b32_e32 v6, v36
	v_mov_b32_e32 v7, v36
	.p2alignl 6, 3212836864

;     __device__ __forceinline__ bool half(const Unit& u) const { return __builtin_amdgcn_readfirstlane((int)cntl[u.e] - u.blk * 256) <= 128; }
; template <int K, class Epi, class Sched, bool ALIGN_EPI>
; __device__ __forceinline__ void gemm_phase(LAS unsigned char* lds, const Gemm g, const Sched& S, const Epi& E) {
;     ...
;         const bool hf = S.half(cur);
;         for (int t = 0; t < nt; t += 2) {
;     ...
;         for (int a = 0; a < 2; ++a)
; #pragma unroll
;             for (int b = 0; b < 2; ++b)
; #pragma unroll
;                 for (int m = 0; m < 4; ++m)
; #pragma unroll
;                     for (int n = 0; n < 2; ++n) acc[a][b][m][n] = (f32x4){0.f, 0.f, 0.f, 0.f};
.LBB0_1934:
	v_lshlrev_b32_e32 v4, 2, v243
	v_add_u32_e32 v4, s8, v4
	ds_read_b32 v4, v4
	v_lshlrev_b32_e32 v5, 8, v6
	s_andn2_b64 vcc, exec, s[46:47]
	s_waitcnt lgkmcnt(0)
	v_sub_u32_e32 v4, v4, v5
	s_nop 0
	v_readfirstlane_b32 s26, v4
	s_cbranch_vccnz .LBB0_1945
	v_mov_b32_e32 v130, v131
	s_mov_b32 s22, s75
	s_mov_b32 s41, s40
	s_mov_b32 s40, s15
	s_mov_b32 s15, s14
	s_mov_b32 s14, s74
	s_cmpk_gt_i32 s26, 0x80
	v_mov_b32_e32 v132, v131
	v_mov_b32_e32 v133, v131
	v_mov_b32_e32 v68, 0
	v_readlane_b32 s74, v254, 50
	v_mov_b64_e32 v[40:41], v[130:131]
	v_mov_b64_e32 v[48:49], v[130:131]
	v_mov_b64_e32 v[56:57], v[130:131]
	v_mov_b64_e32 v[64:65], v[130:131]
	v_mov_b64_e32 v[4:5], v[130:131]
	v_mov_b64_e32 v[12:13], v[130:131]
	v_mov_b64_e32 v[20:21], v[130:131]
	v_mov_b64_e32 v[28:29], v[130:131]
	v_mov_b64_e32 v[36:37], v[130:131]
	v_mov_b64_e32 v[44:45], v[130:131]
	v_mov_b64_e32 v[52:53], v[130:131]
	v_mov_b64_e32 v[60:61], v[130:131]
	v_mov_b64_e32 v[32:33], v[130:131]
	v_mov_b64_e32 v[24:25], v[130:131]
	v_mov_b64_e32 v[16:17], v[130:131]
	v_mov_b64_e32 v[8:9], v[130:131]
	s_mov_b32 s42, s91
	s_mov_b32 s31, s89
	s_mov_b32 s23, s88
	s_mov_b32 s30, s69
	s_mov_b32 s91, s66
	s_mov_b32 s89, s65
	s_mov_b32 s88, s64
	s_cselect_b64 s[64:65], -1, 0
	v_mov_b32_e32 v217, v131
	v_mov_b32_e32 v213, v131
	s_mov_b32 s94, 0
	s_mov_b64 s[66:67], 0x100
	v_readlane_b32 s75, v254, 51
	v_mov_b64_e32 v[42:43], v[132:133]
	v_mov_b64_e32 v[50:51], v[132:133]
	v_mov_b64_e32 v[58:59], v[132:133]
	v_mov_b64_e32 v[66:67], v[132:133]
	v_mov_b64_e32 v[6:7], v[132:133]
	v_mov_b64_e32 v[14:15], v[132:133]
	v_mov_b64_e32 v[22:23], v[132:133]
	v_mov_b64_e32 v[30:31], v[132:133]
	v_mov_b64_e32 v[38:39], v[132:133]
	v_mov_b64_e32 v[46:47], v[132:133]
	v_mov_b64_e32 v[54:55], v[132:133]
	v_mov_b64_e32 v[62:63], v[132:133]
	v_mov_b64_e32 v[34:35], v[132:133]
	v_mov_b64_e32 v[26:27], v[132:133]
	v_mov_b64_e32 v[18:19], v[132:133]
	v_mov_b64_e32 v[10:11], v[132:133]
	v_mov_b32_e32 v69, v68
	v_mov_b32_e32 v70, v68
	v_mov_b32_e32 v71, v68
	v_mov_b32_e32 v80, v68
	v_mov_b32_e32 v81, v68
	v_mov_b32_e32 v82, v68
	v_mov_b32_e32 v83, v68
	v_mov_b32_e32 v88, v68
	v_mov_b32_e32 v89, v68
	v_mov_b32_e32 v90, v68
	v_mov_b32_e32 v91, v68
	v_mov_b32_e32 v96, v68
	v_mov_b32_e32 v97, v68
	v_mov_b32_e32 v98, v68
	v_mov_b32_e32 v99, v68
	v_mov_b32_e32 v104, v68
	v_mov_b32_e32 v105, v68
	v_mov_b32_e32 v106, v68
	v_mov_b32_e32 v107, v68
	v_mov_b32_e32 v112, v68
	v_mov_b32_e32 v113, v68
	v_mov_b32_e32 v114, v68
	v_mov_b32_e32 v115, v68
	v_mov_b32_e32 v120, v68
	v_mov_b32_e32 v121, v68
	v_mov_b32_e32 v122, v68
	v_mov_b32_e32 v123, v68
	v_mov_b32_e32 v138, v68
	v_mov_b32_e32 v139, v68
	v_mov_b32_e32 v140, v68
	v_mov_b32_e32 v141, v68
	v_mov_b32_e32 v72, v68
	v_mov_b32_e32 v73, v68
	v_mov_b32_e32 v74, v68
	v_mov_b32_e32 v75, v68
	v_mov_b32_e32 v76, v68
	v_mov_b32_e32 v77, v68
	v_mov_b32_e32 v78, v68
	v_mov_b32_e32 v79, v68
	v_mov_b32_e32 v84, v68
	v_mov_b32_e32 v85, v68
	v_mov_b32_e32 v86, v68
	v_mov_b32_e32 v87, v68
	v_mov_b32_e32 v92, v68
	v_mov_b32_e32 v93, v68
	v_mov_b32_e32 v94, v68
	v_mov_b32_e32 v95, v68
	v_mov_b32_e32 v100, v68
	v_mov_b32_e32 v101, v68
	v_mov_b32_e32 v102, v68
	v_mov_b32_e32 v103, v68
	v_mov_b32_e32 v108, v68
	v_mov_b32_e32 v109, v68
	v_mov_b32_e32 v110, v68
	v_mov_b32_e32 v111, v68
	v_mov_b32_e32 v116, v68
	v_mov_b32_e32 v117, v68
	v_mov_b32_e32 v118, v68
	v_mov_b32_e32 v119, v68
	v_mov_b32_e32 v124, v68
	v_mov_b32_e32 v125, v68
	v_mov_b32_e32 v126, v68
	v_mov_b32_e32 v127, v68
	s_branch .LBB0_1937
	.p2alignl 6, 3212836864

; #define PG8_STAGE(bufoff, gbase, voff) do { _Pragma("unroll") for (int _i = 0; _i < 2; ++_i) \
;         __builtin_amdgcn_global_load_lds((const unsigned*)((const char*)(gbase) + (voff)[_i]), (LAS unsigned*)(lds + (bufoff) + ldsw + _i * 8192), 16, 0, 0); } while (0)
; #define PG8_WAIT_V(n) asm volatile("s_waitcnt vmcnt(" #n ")" ::: "memory")
; #define PG8_BAR __builtin_amdgcn_s_barrier()
; #define PG8_AOFF(dst, u) do { int _t = tid; asm volatile("" : "+v"(_t)); _Pragma("unroll") for (int _i = 0; _i < 2; ++_i) { int _R, _C; stage_rc(_t * 16 + _i * 8192, _R, _C); _Pragma("unroll") for (int _h = 0; _h < 2; ++_h) dst[_h][_i] = ((unsigned)S.arow(u, _h * HALF + _R) * (unsigned)Kr + (unsigned)_C) * 2u; } } while (0)
; template <int K, class Epi, class Sched, bool ALIGN_EPI>
; __device__ __forceinline__ void gemm_phase(LAS unsigned char* lds, const Gemm g, const Sched& S, const Epi& E) {
;     ...
;     f32x4 acc[2][2][4][2];
; #pragma unroll
;     for (int a = 0; a < 2; ++a)
; #pragma unroll
;         for (int b = 0; b < 2; ++b)
; #pragma unroll
;             for (int m = 0; m < 4; ++m)
; #pragma unroll
;                 for (int n = 0; n < 2; ++n) acc[a][b][m][n] = (f32x4){0.f, 0.f, 0.f, 0.f};
;     bf16x8 At[4][2], B0[2][2], B1[2][2];
;     unsigned ca[2][2], na[2][2];
;     PG8_AOFF(ca, cur);
;     const char* gA = (const char*)g.A;
;     const char* cB = (const char*)g.Bt + (size_t)cur.pn * tstep;
;     PG8_STAGE(PG8_SB(0, 0), cB, voffB); PG8_STAGE(PG8_SB(0, 1), cB + hstep, voffB); PG8_STAGE(PG8_SA(0, 0), gA, ca[0]); PG8_STAGE(PG8_SA(0, 1), gA, ca[1]);
;     if (wr == 1) PG8_BAR;
;     PG8_WAIT_V(2); PG8_BAR;
;     PG8_STAGE(PG8_SB(1, 0), cB + kstep, voffB); PG8_STAGE(PG8_SA(1, 0), gA + kstep, ca[0]); PG8_STAGE(PG8_SB(1, 1), cB + hstep + kstep, voffB);
;     PG8_WAIT_V(6); PG8_BAR;
.LBB0_1962:
	v_mov_b32_e32 v129, v131
	v_lshl_add_u64 v[4:5], s[14:15], 0, v[130:131]
	v_lshl_add_u64 v[8:9], s[24:25], 0, v[130:131]
	v_lshl_add_u64 v[10:11], s[24:25], 0, v[128:129]
	s_add_i32 s24, s6, s40
	v_lshl_add_u64 v[6:7], s[14:15], 0, v[128:129]
	v_mov_b32_e32 v133, v131
	v_lshl_add_u64 v[4:5], v[4:5], 0, s[10:11]
	s_mov_b32 m0, s24
	s_add_i32 s25, s24, 0x2000
	v_lshl_add_u64 v[12:13], s[0:1], 0, v[132:133]
	v_mov_b32_e32 v145, v131
	s_waitcnt vmcnt(2)
	s_barrier
	global_load_lds_dwordx4 v[4:5], off
	v_lshl_add_u64 v[4:5], v[6:7], 0, s[10:11]
	s_mov_b32 m0, s25
	s_add_i32 s37, s33, 0x8000
	v_lshl_add_u64 v[14:15], s[0:1], 0, v[144:145]
	global_load_lds_dwordx4 v[4:5], off
	v_lshl_add_u64 v[4:5], v[12:13], 0, s[10:11]
	s_mov_b32 m0, s37
	s_add_i32 s38, s33, 0xa000
	global_load_lds_dwordx4 v[4:5], off
	v_lshl_add_u64 v[4:5], v[14:15], 0, s[10:11]
	s_mov_b32 m0, s38
	s_add_i32 s40, s7, s40
	global_load_lds_dwordx4 v[4:5], off
	v_lshl_add_u64 v[4:5], v[8:9], 0, s[10:11]
	s_mov_b32 m0, s40
	s_add_i32 s41, s40, 0x2000
	global_load_lds_dwordx4 v[4:5], off
	v_lshl_add_u64 v[4:5], v[10:11], 0, s[10:11]
	s_mov_b32 m0, s41
	s_and_b32 s21, s20, 3
	global_load_lds_dwordx4 v[4:5], off
	s_waitcnt vmcnt(6)
	s_lshl_b32 s20, s44, 6
	v_mov_b32_e32 v7, 0
	v_and_b32_e32 v3, 15, v1
	v_bfe_u32 v1, v1, 4, 2
	s_cmp_lt_i32 s18, 64
	v_mov_b32_e32 v6, v7
	v_mov_b32_e32 v5, v7
	v_mov_b32_e32 v4, v7
	v_mov_b32_e32 v11, v7
	v_mov_b32_e32 v10, v7
	v_mov_b32_e32 v9, v7
	v_mov_b32_e32 v8, v7
	v_mov_b32_e32 v23, v7
	v_mov_b32_e32 v22, v7
	v_mov_b32_e32 v21, v7
	v_mov_b32_e32 v20, v7
	v_mov_b32_e32 v27, v7
	v_mov_b32_e32 v26, v7
	v_mov_b32_e32 v25, v7
	v_mov_b32_e32 v24, v7
	v_mov_b32_e32 v141, v7
	v_mov_b32_e32 v140, v7
	v_mov_b32_e32 v139, v7
	v_mov_b32_e32 v138, v7
	v_mov_b32_e32 v127, v7
	v_mov_b32_e32 v126, v7
	v_mov_b32_e32 v125, v7
	v_mov_b32_e32 v124, v7
	v_mov_b32_e32 v115, v7
	v_mov_b32_e32 v114, v7
	v_mov_b32_e32 v113, v7
	v_mov_b32_e32 v112, v7
	v_mov_b32_e32 v111, v7
	v_mov_b32_e32 v110, v7
	v_mov_b32_e32 v109, v7
	v_mov_b32_e32 v108, v7
	v_mov_b32_e32 v99, v7
	v_mov_b32_e32 v98, v7
	v_mov_b32_e32 v97, v7
	v_mov_b32_e32 v96, v7
	v_mov_b32_e32 v95, v7
	v_mov_b32_e32 v94, v7
	v_mov_b32_e32 v93, v7
	v_mov_b32_e32 v92, v7
	v_mov_b32_e32 v83, v7
	v_mov_b32_e32 v82, v7
	v_mov_b32_e32 v81, v7
	v_mov_b32_e32 v80, v7
	v_mov_b32_e32 v79, v7
	v_mov_b32_e32 v78, v7
	v_mov_b32_e32 v77, v7
	v_mov_b32_e32 v76, v7
	v_mov_b32_e32 v123, v7
	v_mov_b32_e32 v122, v7
	v_mov_b32_e32 v121, v7
	v_mov_b32_e32 v120, v7
	v_mov_b32_e32 v119, v7
	v_mov_b32_e32 v118, v7
	v_mov_b32_e32 v117, v7
	v_mov_b32_e32 v116, v7
	v_mov_b32_e32 v107, v7
	v_mov_b32_e32 v106, v7
	v_mov_b32_e32 v105, v7
	v_mov_b32_e32 v104, v7
	v_mov_b32_e32 v103, v7
	v_mov_b32_e32 v102, v7
	v_mov_b32_e32 v101, v7
	v_mov_b32_e32 v100, v7
	v_mov_b32_e32 v91, v7
	v_mov_b32_e32 v90, v7
	v_mov_b32_e32 v89, v7
	v_mov_b32_e32 v88, v7
	v_mov_b32_e32 v87, v7
	v_mov_b32_e32 v86, v7
	v_mov_b32_e32 v85, v7
	v_mov_b32_e32 v84, v7
	v_mov_b32_e32 v75, v7
	v_mov_b32_e32 v74, v7
	v_mov_b32_e32 v73, v7
	v_mov_b32_e32 v72, v7
	v_mov_b32_e32 v71, v7
	v_mov_b32_e32 v70, v7
	v_mov_b32_e32 v69, v7
	v_mov_b32_e32 v68, v7
	v_mov_b32_e32 v67, v7
	v_mov_b32_e32 v66, v7
	v_mov_b32_e32 v65, v7
	v_mov_b32_e32 v64, v7
	v_mov_b32_e32 v63, v7
	v_mov_b32_e32 v62, v7
	v_mov_b32_e32 v61, v7
	v_mov_b32_e32 v60, v7
	v_mov_b32_e32 v51, v7
	v_mov_b32_e32 v50, v7
	v_mov_b32_e32 v49, v7
	v_mov_b32_e32 v48, v7
	v_mov_b32_e32 v47, v7
	v_mov_b32_e32 v46, v7
	v_mov_b32_e32 v45, v7
	v_mov_b32_e32 v44, v7
	v_mov_b32_e32 v35, v7
	v_mov_b32_e32 v34, v7
	v_mov_b32_e32 v33, v7
	v_mov_b32_e32 v32, v7
	v_mov_b32_e32 v31, v7
	v_mov_b32_e32 v30, v7
	v_mov_b32_e32 v29, v7
	v_mov_b32_e32 v28, v7
	v_mov_b32_e32 v19, v7
	v_mov_b32_e32 v18, v7
	v_mov_b32_e32 v17, v7
	v_mov_b32_e32 v16, v7
	v_mov_b32_e32 v15, v7
	v_mov_b32_e32 v14, v7
	v_mov_b32_e32 v13, v7
	v_mov_b32_e32 v12, v7
	v_mov_b32_e32 v59, v7
	v_mov_b32_e32 v58, v7
	v_mov_b32_e32 v57, v7
	v_mov_b32_e32 v56, v7
	v_mov_b32_e32 v55, v7
	v_mov_b32_e32 v54, v7
	v_mov_b32_e32 v53, v7
	v_mov_b32_e32 v52, v7
	v_mov_b32_e32 v43, v7
	v_mov_b32_e32 v42, v7
	v_mov_b32_e32 v41, v7
	v_mov_b32_e32 v40, v7
	v_mov_b32_e32 v39, v7
	v_mov_b32_e32 v38, v7
	v_mov_b32_e32 v37, v7
	v_mov_b32_e32 v36, v7
	s_barrier
; template <int K, class Epi, class Sched, bool ALIGN_EPI>
; __device__ __forceinline__ void gemm_phase(LAS unsigned char* lds, const Gemm g, const Sched& S, const Epi& E) {
;     ...
;     const int tid = tid_, wid = __builtin_amdgcn_readfirstlane(tid >> 6), lane = tid & 63, wr = wid >> 2, wc = wid & 3, fr = lane & 15, fq = lane >> 4;
;     int Kr = K; asm volatile("" : "+s"(Kr));
;     const int nt = Kr / BK;
;     unsigned voffB[2];
; #pragma unroll
;     for (int i = 0; i < 2; ++i) { int R_, C_; stage_rc(tid * 16 + i * 8192, R_, C_); const int Rb = (R_ & ~31) + perm32(R_ & 31); voffB[i] = (unsigned)(Rb * Kr + C_) * 2u; }
;     const size_t kstep = (size_t)(BK * 2);
;     const size_t hstep = (size_t)HALF * Kr * 2;
;     const size_t tstep = 2 * hstep;
;     const unsigned ldsw = (unsigned)wid * 1024u;
;     const int aoff = lds_byte(wr * 64 + fr, fq * 8), boff = lds_byte(wc * 32 + fr, fq * 8);
;     ...
;     f32x4 acc[2][2][4][2];
; #pragma unroll
;     for (int a = 0; a < 2; ++a)
; #pragma unroll
;         for (int b = 0; b < 2; ++b)
; #pragma unroll
;             for (int m = 0; m < 4; ++m)
; #pragma unroll
;                 for (int n = 0; n < 2; ++n) acc[a][b][m][n] = (f32x4){0.f, 0.f, 0.f, 0.f};
	s_cbranch_scc1 .LBB0_1965
	s_lshr_b32 s19, s19, 26
	s_add_i32 s19, s18, s19
	v_or_b32_e32 v4, s20, v3
	s_ashr_i32 s42, s19, 6
	v_lshlrev_b32_e32 v5, 4, v1
	v_lshlrev_b32_e32 v6, 6, v4
	s_movk_i32 s19, 0x3c0
	v_lshlrev_b32_e32 v4, 2, v4
	v_and_or_b32 v6, v6, s19, v5
	s_lshl_b32 s19, s44, 13
	v_and_b32_e32 v4, 32, v4
	v_bitop3_b32 v6, v6, s19, v4 bitop3:0xde
	v_lshl_or_b32 v4, v3, 6, v5
	v_lshlrev_b32_e32 v5, 2, v3
	s_lshl_b32 s19, s21, 12
	v_and_b32_e32 v5, 32, v5
	v_bitop3_b32 v152, v4, s19, v5 bitop3:0xde
	v_add_u32_e32 v4, s8, v149
	s_movk_i32 s19, 0x80
	s_add_i32 s43, s42, -2
	v_add3_u32 v4, v4, v148, s19
	v_mad_u64_u32 v[4:5], s[44:45], s18, v4, v[134:135]
	s_add_u32 s22, s30, s22
	v_add_lshl_u32 v4, v4, v151, 1
	v_mov_b32_e32 v5, v131
	s_addc_u32 s23, s31, s23
	v_lshl_add_u64 v[148:149], s[22:23], 0, v[4:5]
	v_add_u32_e32 v4, s8, v154
	v_add3_u32 v4, v4, v153, s19
	v_mad_u64_u32 v[4:5], s[18:19], s18, v4, v[150:151]
	v_add_lshl_u32 v4, v4, v155, 1
	v_mov_b32_e32 v5, v131
	v_mov_b32_e32 v36, 0
	v_mov_b32_e32 v143, v131
	v_mov_b32_e32 v147, v131
	v_lshl_add_u64 v[150:151], s[22:23], 0, v[4:5]
	s_mov_b32 s22, 0
	s_mov_b64 s[18:19], 0x11000080
	v_add_u32_e32 v134, s96, v6
	v_mov_b32_e32 v37, v36
	v_mov_b32_e32 v38, v36
	v_mov_b32_e32 v39, v36
	v_mov_b32_e32 v40, v36
	v_mov_b32_e32 v41, v36
	v_mov_b32_e32 v42, v36
	v_mov_b32_e32 v43, v36
	v_mov_b32_e32 v52, v36
	v_mov_b32_e32 v53, v36
	v_mov_b32_e32 v54, v36
	v_mov_b32_e32 v55, v36
	v_mov_b32_e32 v56, v36
	v_mov_b32_e32 v57, v36
	v_mov_b32_e32 v58, v36
	v_mov_b32_e32 v59, v36
	v_mov_b32_e32 v12, v36
	v_mov_b32_e32 v13, v36
	v_mov_b32_e32 v14, v36
	v_mov_b32_e32 v15, v36
	v_mov_b32_e32 v16, v36
	v_mov_b32_e32 v17, v36
	v_mov_b32_e32 v18, v36
	v_mov_b32_e32 v19, v36
	v_mov_b32_e32 v28, v36
	v_mov_b32_e32 v29, v36
	v_mov_b32_e32 v30, v36
	v_mov_b32_e32 v31, v36
	v_mov_b32_e32 v32, v36
	v_mov_b32_e32 v33, v36
	v_mov_b32_e32 v34, v36
	v_mov_b32_e32 v35, v36
	v_mov_b32_e32 v44, v36
	v_mov_b32_e32 v45, v36
	v_mov_b32_e32 v46, v36
	v_mov_b32_e32 v47, v36
	v_mov_b32_e32 v48, v36
	v_mov_b32_e32 v49, v36
	v_mov_b32_e32 v50, v36
	v_mov_b32_e32 v51, v36
	v_mov_b32_e32 v60, v36
	v_mov_b32_e32 v61, v36
	v_mov_b32_e32 v62, v36
	v_mov_b32_e32 v63, v36
	v_mov_b32_e32 v64, v36
	v_mov_b32_e32 v65, v36
	v_mov_b32_e32 v66, v36
	v_mov_b32_e32 v67, v36
	v_mov_b32_e32 v68, v36
	v_mov_b32_e32 v69, v36
	v_mov_b32_e32 v70, v36
	v_mov_b32_e32 v71, v36
	v_mov_b32_e32 v72, v36
	v_mov_b32_e32 v73, v36
	v_mov_b32_e32 v74, v36
	v_mov_b32_e32 v75, v36
	v_mov_b32_e32 v84, v36
	v_mov_b32_e32 v85, v36
	v_mov_b32_e32 v86, v36
	v_mov_b32_e32 v87, v36
	v_mov_b32_e32 v88, v36
	v_mov_b32_e32 v89, v36
	v_mov_b32_e32 v90, v36
	v_mov_b32_e32 v91, v36
	v_mov_b32_e32 v100, v36
	v_mov_b32_e32 v101, v36
	v_mov_b32_e32 v102, v36
	v_mov_b32_e32 v103, v36
	v_mov_b32_e32 v104, v36
	v_mov_b32_e32 v105, v36
	v_mov_b32_e32 v106, v36
	v_mov_b32_e32 v107, v36
	v_mov_b32_e32 v116, v36
	v_mov_b32_e32 v117, v36
	v_mov_b32_e32 v118, v36
	v_mov_b32_e32 v119, v36
	v_mov_b32_e32 v120, v36
	v_mov_b32_e32 v121, v36
	v_mov_b32_e32 v122, v36
	v_mov_b32_e32 v123, v36
	v_mov_b32_e32 v76, v36
	v_mov_b32_e32 v77, v36
	v_mov_b32_e32 v78, v36
	v_mov_b32_e32 v79, v36
	v_mov_b32_e32 v80, v36
	v_mov_b32_e32 v81, v36
	v_mov_b32_e32 v82, v36
	v_mov_b32_e32 v83, v36
	v_mov_b32_e32 v92, v36
	v_mov_b32_e32 v93, v36
	v_mov_b32_e32 v94, v36
	v_mov_b32_e32 v95, v36
	v_mov_b32_e32 v96, v36
	v_mov_b32_e32 v97, v36
	v_mov_b32_e32 v98, v36
	v_mov_b32_e32 v99, v36
	v_mov_b32_e32 v108, v36
	v_mov_b32_e32 v109, v36
	v_mov_b32_e32 v110, v36
	v_mov_b32_e32 v111, v36
	v_mov_b32_e32 v112, v36
	v_mov_b32_e32 v113, v36
	v_mov_b32_e32 v114, v36
	v_mov_b32_e32 v115, v36
	v_mov_b32_e32 v124, v36
	v_mov_b32_e32 v125, v36
	v_mov_b32_e32 v126, v36
	v_mov_b32_e32 v127, v36
	v_mov_b32_e32 v138, v36
	v_mov_b32_e32 v139, v36
	v_mov_b32_e32 v140, v36
	v_mov_b32_e32 v141, v36
	v_mov_b32_e32 v24, v36
	v_mov_b32_e32 v25, v36
	v_mov_b32_e32 v26, v36
	v_mov_b32_e32 v27, v36
	v_mov_b32_e32 v20, v36
	v_mov_b32_e32 v21, v36
	v_mov_b32_e32 v22, v36
	v_mov_b32_e32 v23, v36
	v_mov_b32_e32 v8, v36
	v_mov_b32_e32 v9, v36
	v_mov_b32_e32 v10, v36
	v_mov_b32_e32 v11, v36
	v_mov_b32_e32 v4, v36
	v_mov_b32_e32 v5, v36
	v_mov_b32_e32 v6, v36
	v_mov_b32_e32 v7, v36
	.p2alignl 6, 3212836864

;     __device__ __forceinline__ bool half(const Unit& u) const { return __builtin_amdgcn_readfirstlane((int)cntl[u.e] - u.blk * 256) <= 128; }
; template <int K, class Epi, class Sched, bool ALIGN_EPI>
; __device__ __forceinline__ void gemm_phase(LAS unsigned char* lds, const Gemm g, const Sched& S, const Epi& E) {
;     ...
;         const bool hf = S.half(cur);
;         for (int t = 0; t < nt; t += 2) {
;     ...
;         for (int a = 0; a < 2; ++a)
; #pragma unroll
;             for (int b = 0; b < 2; ++b)
; #pragma unroll
;                 for (int m = 0; m < 4; ++m)
; #pragma unroll
;                     for (int n = 0; n < 2; ++n) acc[a][b][m][n] = (f32x4){0.f, 0.f, 0.f, 0.f};
.LBB0_2060:
	v_lshlrev_b32_e32 v4, 2, v249
	v_add_u32_e32 v4, s78, v4
	ds_read_b32 v4, v4
	v_lshlrev_b32_e32 v5, 8, v6
	s_andn2_b64 vcc, exec, s[44:45]
	s_waitcnt lgkmcnt(0)
	v_sub_u32_e32 v4, v4, v5
	s_nop 0
	v_readfirstlane_b32 s26, v4
	s_cbranch_vccnz .LBB0_2071
	v_mov_b32_e32 v130, v131
	s_cmpk_gt_i32 s26, 0x80
	v_mov_b32_e32 v132, v131
	v_mov_b32_e32 v133, v131
	s_waitcnt vmcnt(0)
	v_mov_b32_e32 v68, 0
	v_mov_b64_e32 v[36:37], v[130:131]
	v_mov_b64_e32 v[40:41], v[130:131]
	v_mov_b64_e32 v[52:53], v[130:131]
	v_mov_b64_e32 v[56:57], v[130:131]
	v_mov_b64_e32 v[12:13], v[130:131]
	v_mov_b64_e32 v[16:17], v[130:131]
	v_mov_b64_e32 v[28:29], v[130:131]
	v_mov_b64_e32 v[32:33], v[130:131]
	v_mov_b64_e32 v[44:45], v[130:131]
	v_mov_b64_e32 v[48:49], v[130:131]
	v_mov_b64_e32 v[60:61], v[130:131]
	v_mov_b64_e32 v[64:65], v[130:131]
	v_mov_b64_e32 v[24:25], v[130:131]
	v_mov_b64_e32 v[20:21], v[130:131]
	v_mov_b64_e32 v[8:9], v[130:131]
	v_mov_b64_e32 v[4:5], v[130:131]
	s_mov_b32 s53, s64
	s_cselect_b64 s[64:65], -1, 0
	v_mov_b32_e32 v217, v131
	v_mov_b32_e32 v213, v131
	s_mov_b32 s52, 0
	s_mov_b64 s[66:67], 0x100
	s_mov_b64 s[74:75], s[42:43]
	v_mov_b64_e32 v[38:39], v[132:133]
	v_mov_b64_e32 v[42:43], v[132:133]
	v_mov_b64_e32 v[54:55], v[132:133]
	v_mov_b64_e32 v[58:59], v[132:133]
	v_mov_b64_e32 v[14:15], v[132:133]
	v_mov_b64_e32 v[18:19], v[132:133]
	v_mov_b64_e32 v[30:31], v[132:133]
	v_mov_b64_e32 v[34:35], v[132:133]
	v_mov_b64_e32 v[46:47], v[132:133]
	v_mov_b64_e32 v[50:51], v[132:133]
	v_mov_b64_e32 v[62:63], v[132:133]
	v_mov_b64_e32 v[66:67], v[132:133]
	v_mov_b64_e32 v[26:27], v[132:133]
	v_mov_b64_e32 v[22:23], v[132:133]
	v_mov_b64_e32 v[10:11], v[132:133]
	v_mov_b64_e32 v[6:7], v[132:133]
	v_mov_b32_e32 v69, v68
	v_mov_b32_e32 v70, v68
	v_mov_b32_e32 v71, v68
	v_mov_b32_e32 v72, v68
	v_mov_b32_e32 v73, v68
	v_mov_b32_e32 v74, v68
	v_mov_b32_e32 v75, v68
	v_mov_b32_e32 v84, v68
	v_mov_b32_e32 v85, v68
	v_mov_b32_e32 v86, v68
	v_mov_b32_e32 v87, v68
	v_mov_b32_e32 v88, v68
	v_mov_b32_e32 v89, v68
	v_mov_b32_e32 v90, v68
	v_mov_b32_e32 v91, v68
	v_mov_b32_e32 v100, v68
	v_mov_b32_e32 v101, v68
	v_mov_b32_e32 v102, v68
	v_mov_b32_e32 v103, v68
	v_mov_b32_e32 v104, v68
	v_mov_b32_e32 v105, v68
	v_mov_b32_e32 v106, v68
	v_mov_b32_e32 v107, v68
	v_mov_b32_e32 v116, v68
	v_mov_b32_e32 v117, v68
	v_mov_b32_e32 v118, v68
	v_mov_b32_e32 v119, v68
	v_mov_b32_e32 v120, v68
	v_mov_b32_e32 v121, v68
	v_mov_b32_e32 v122, v68
	v_mov_b32_e32 v123, v68
	v_mov_b32_e32 v76, v68
	v_mov_b32_e32 v77, v68
	v_mov_b32_e32 v78, v68
	v_mov_b32_e32 v79, v68
	v_mov_b32_e32 v80, v68
	v_mov_b32_e32 v81, v68
	v_mov_b32_e32 v82, v68
	v_mov_b32_e32 v83, v68
	v_mov_b32_e32 v92, v68
	v_mov_b32_e32 v93, v68
	v_mov_b32_e32 v94, v68
	v_mov_b32_e32 v95, v68
	v_mov_b32_e32 v96, v68
	v_mov_b32_e32 v97, v68
	v_mov_b32_e32 v98, v68
	v_mov_b32_e32 v99, v68
	v_mov_b32_e32 v108, v68
	v_mov_b32_e32 v109, v68
	v_mov_b32_e32 v110, v68
	v_mov_b32_e32 v111, v68
	v_mov_b32_e32 v112, v68
	v_mov_b32_e32 v113, v68
	v_mov_b32_e32 v114, v68
	v_mov_b32_e32 v115, v68
	v_mov_b32_e32 v124, v68
	v_mov_b32_e32 v125, v68
	v_mov_b32_e32 v126, v68
	v_mov_b32_e32 v127, v68
	v_mov_b32_e32 v138, v68
	v_mov_b32_e32 v139, v68
	v_mov_b32_e32 v140, v68
	v_mov_b32_e32 v141, v68
	s_branch .LBB0_2063
	.p2alignl 6, 3212836864

; #define PG8_STAGE(bufoff, gbase, voff) do { _Pragma("unroll") for (int _i = 0; _i < 2; ++_i) \
;         __builtin_amdgcn_global_load_lds((const unsigned*)((const char*)(gbase) + (voff)[_i]), (LAS unsigned*)(lds + (bufoff) + ldsw + _i * 8192), 16, 0, 0); } while (0)
; #define PG8_WAIT_V(n) asm volatile("s_waitcnt vmcnt(" #n ")" ::: "memory")
; #define PG8_BAR __builtin_amdgcn_s_barrier()
; #define PG8_AOFF(dst, u) do { int _t = tid; asm volatile("" : "+v"(_t)); _Pragma("unroll") for (int _i = 0; _i < 2; ++_i) { int _R, _C; stage_rc(_t * 16 + _i * 8192, _R, _C); _Pragma("unroll") for (int _h = 0; _h < 2; ++_h) dst[_h][_i] = ((unsigned)S.arow(u, _h * HALF + _R) * (unsigned)Kr + (unsigned)_C) * 2u; } } while (0)
; template <int K, class Epi, class Sched, bool ALIGN_EPI>
; __device__ __forceinline__ void gemm_phase(LAS unsigned char* lds, const Gemm g, const Sched& S, const Epi& E) {
;     ...
;     f32x4 acc[2][2][4][2];
; #pragma unroll
;     for (int a = 0; a < 2; ++a)
; #pragma unroll
;         for (int b = 0; b < 2; ++b)
; #pragma unroll
;             for (int m = 0; m < 4; ++m)
; #pragma unroll
;                 for (int n = 0; n < 2; ++n) acc[a][b][m][n] = (f32x4){0.f, 0.f, 0.f, 0.f};
;     bf16x8 At[4][2], B0[2][2], B1[2][2];
;     unsigned ca[2][2], na[2][2];
;     PG8_AOFF(ca, cur);
;     const char* gA = (const char*)g.A;
;     const char* cB = (const char*)g.Bt + (size_t)cur.pn * tstep;
;     PG8_STAGE(PG8_SB(0, 0), cB, voffB); PG8_STAGE(PG8_SB(0, 1), cB + hstep, voffB); PG8_STAGE(PG8_SA(0, 0), gA, ca[0]); PG8_STAGE(PG8_SA(0, 1), gA, ca[1]);
;     if (wr == 1) PG8_BAR;
;     PG8_WAIT_V(2); PG8_BAR;
;     PG8_STAGE(PG8_SB(1, 0), cB + kstep, voffB); PG8_STAGE(PG8_SA(1, 0), gA + kstep, ca[0]); PG8_STAGE(PG8_SB(1, 1), cB + hstep + kstep, voffB);
;     PG8_WAIT_V(6); PG8_BAR;
.LBB0_2168:
	v_mov_b32_e32 v129, v131
	v_lshl_add_u64 v[8:9], s[26:27], 0, v[130:131]
	v_lshl_add_u64 v[10:11], s[26:27], 0, v[128:129]
	s_add_i32 s26, s2, 0x18000
	v_lshl_add_u64 v[4:5], s[18:19], 0, v[130:131]
	s_add_i32 s27, s26, s41
	v_lshl_add_u64 v[6:7], s[18:19], 0, v[128:129]
	v_mov_b32_e32 v133, v131
	v_lshl_add_u64 v[4:5], v[4:5], 0, s[10:11]
	s_mov_b32 m0, s27
	s_add_i32 s36, s27, 0x2000
	v_lshl_add_u64 v[12:13], s[12:13], 0, v[132:133]
	v_mov_b32_e32 v145, v131
	s_waitcnt vmcnt(2)
	s_barrier
	global_load_lds_dwordx4 v[4:5], off
	v_lshl_add_u64 v[4:5], v[6:7], 0, s[10:11]
	s_mov_b32 m0, s36
	s_add_i32 s37, s31, 0x8000
	v_lshl_add_u64 v[14:15], s[12:13], 0, v[144:145]
	global_load_lds_dwordx4 v[4:5], off
	v_lshl_add_u64 v[4:5], v[12:13], 0, s[10:11]
	s_mov_b32 m0, s37
	s_add_i32 s38, s31, 0xa000
	s_add_i32 s40, s2, 0x1c000
	global_load_lds_dwordx4 v[4:5], off
	v_lshl_add_u64 v[4:5], v[14:15], 0, s[10:11]
	s_mov_b32 m0, s38
	s_add_i32 s41, s40, s41
	global_load_lds_dwordx4 v[4:5], off
	v_lshl_add_u64 v[4:5], v[8:9], 0, s[10:11]
	s_mov_b32 m0, s41
	s_add_i32 s42, s41, 0x2000
	global_load_lds_dwordx4 v[4:5], off
	v_lshl_add_u64 v[4:5], v[10:11], 0, s[10:11]
	s_mov_b32 m0, s42
	s_and_b32 s7, s6, 3
	global_load_lds_dwordx4 v[4:5], off
	s_waitcnt vmcnt(6)
	s_lshl_b32 s6, s45, 6
	v_mov_b32_e32 v7, 0
	v_and_b32_e32 v3, 15, v1
	v_bfe_u32 v1, v1, 4, 2
	s_cmp_lt_i32 s22, 64
	v_mov_b32_e32 v6, v7
	v_mov_b32_e32 v5, v7
	v_mov_b32_e32 v4, v7
	v_mov_b32_e32 v11, v7
	v_mov_b32_e32 v10, v7
	v_mov_b32_e32 v9, v7
	v_mov_b32_e32 v8, v7
	v_mov_b32_e32 v23, v7
	v_mov_b32_e32 v22, v7
	v_mov_b32_e32 v21, v7
	v_mov_b32_e32 v20, v7
	v_mov_b32_e32 v27, v7
	v_mov_b32_e32 v26, v7
	v_mov_b32_e32 v25, v7
	v_mov_b32_e32 v24, v7
	v_mov_b32_e32 v141, v7
	v_mov_b32_e32 v140, v7
	v_mov_b32_e32 v139, v7
	v_mov_b32_e32 v138, v7
	v_mov_b32_e32 v127, v7
	v_mov_b32_e32 v126, v7
	v_mov_b32_e32 v125, v7
	v_mov_b32_e32 v124, v7
	v_mov_b32_e32 v115, v7
	v_mov_b32_e32 v114, v7
	v_mov_b32_e32 v113, v7
	v_mov_b32_e32 v112, v7
	v_mov_b32_e32 v111, v7
	v_mov_b32_e32 v110, v7
	v_mov_b32_e32 v109, v7
	v_mov_b32_e32 v108, v7
	v_mov_b32_e32 v99, v7
	v_mov_b32_e32 v98, v7
	v_mov_b32_e32 v97, v7
	v_mov_b32_e32 v96, v7
	v_mov_b32_e32 v95, v7
	v_mov_b32_e32 v94, v7
	v_mov_b32_e32 v93, v7
	v_mov_b32_e32 v92, v7
	v_mov_b32_e32 v83, v7
	v_mov_b32_e32 v82, v7
	v_mov_b32_e32 v81, v7
	v_mov_b32_e32 v80, v7
	v_mov_b32_e32 v79, v7
	v_mov_b32_e32 v78, v7
	v_mov_b32_e32 v77, v7
	v_mov_b32_e32 v76, v7
	v_mov_b32_e32 v123, v7
	v_mov_b32_e32 v122, v7
	v_mov_b32_e32 v121, v7
	v_mov_b32_e32 v120, v7
	v_mov_b32_e32 v119, v7
	v_mov_b32_e32 v118, v7
	v_mov_b32_e32 v117, v7
	v_mov_b32_e32 v116, v7
	v_mov_b32_e32 v107, v7
	v_mov_b32_e32 v106, v7
	v_mov_b32_e32 v105, v7
	v_mov_b32_e32 v104, v7
	v_mov_b32_e32 v103, v7
	v_mov_b32_e32 v102, v7
	v_mov_b32_e32 v101, v7
	v_mov_b32_e32 v100, v7
	v_mov_b32_e32 v91, v7
	v_mov_b32_e32 v90, v7
	v_mov_b32_e32 v89, v7
	v_mov_b32_e32 v88, v7
	v_mov_b32_e32 v87, v7
	v_mov_b32_e32 v86, v7
	v_mov_b32_e32 v85, v7
	v_mov_b32_e32 v84, v7
	v_mov_b32_e32 v75, v7
	v_mov_b32_e32 v74, v7
	v_mov_b32_e32 v73, v7
	v_mov_b32_e32 v72, v7
	v_mov_b32_e32 v71, v7
	v_mov_b32_e32 v70, v7
	v_mov_b32_e32 v69, v7
	v_mov_b32_e32 v68, v7
	v_mov_b32_e32 v67, v7
	v_mov_b32_e32 v66, v7
	v_mov_b32_e32 v65, v7
	v_mov_b32_e32 v64, v7
	v_mov_b32_e32 v63, v7
	v_mov_b32_e32 v62, v7
	v_mov_b32_e32 v61, v7
	v_mov_b32_e32 v60, v7
	v_mov_b32_e32 v51, v7
	v_mov_b32_e32 v50, v7
	v_mov_b32_e32 v49, v7
	v_mov_b32_e32 v48, v7
	v_mov_b32_e32 v47, v7
	v_mov_b32_e32 v46, v7
	v_mov_b32_e32 v45, v7
	v_mov_b32_e32 v44, v7
	v_mov_b32_e32 v35, v7
	v_mov_b32_e32 v34, v7
	v_mov_b32_e32 v33, v7
	v_mov_b32_e32 v32, v7
	v_mov_b32_e32 v31, v7
	v_mov_b32_e32 v30, v7
	v_mov_b32_e32 v29, v7
	v_mov_b32_e32 v28, v7
	v_mov_b32_e32 v19, v7
	v_mov_b32_e32 v18, v7
	v_mov_b32_e32 v17, v7
	v_mov_b32_e32 v16, v7
	v_mov_b32_e32 v15, v7
	v_mov_b32_e32 v14, v7
	v_mov_b32_e32 v13, v7
	v_mov_b32_e32 v12, v7
	v_mov_b32_e32 v59, v7
	v_mov_b32_e32 v58, v7
	v_mov_b32_e32 v57, v7
	v_mov_b32_e32 v56, v7
	v_mov_b32_e32 v55, v7
	v_mov_b32_e32 v54, v7
	v_mov_b32_e32 v53, v7
	v_mov_b32_e32 v52, v7
	v_mov_b32_e32 v43, v7
	v_mov_b32_e32 v42, v7
	v_mov_b32_e32 v41, v7
	v_mov_b32_e32 v40, v7
	v_mov_b32_e32 v39, v7
	v_mov_b32_e32 v38, v7
	v_mov_b32_e32 v37, v7
	v_mov_b32_e32 v36, v7
	s_barrier
; template <int K, class Epi, class Sched, bool ALIGN_EPI>
; __device__ __forceinline__ void gemm_phase(LAS unsigned char* lds, const Gemm g, const Sched& S, const Epi& E) {
;     ...
;     const int tid = tid_, wid = __builtin_amdgcn_readfirstlane(tid >> 6), lane = tid & 63, wr = wid >> 2, wc = wid & 3, fr = lane & 15, fq = lane >> 4;
;     int Kr = K; asm volatile("" : "+s"(Kr));
;     const int nt = Kr / BK;
;     unsigned voffB[2];
; #pragma unroll
;     for (int i = 0; i < 2; ++i) { int R_, C_; stage_rc(tid * 16 + i * 8192, R_, C_); const int Rb = (R_ & ~31) + perm32(R_ & 31); voffB[i] = (unsigned)(Rb * Kr + C_) * 2u; }
;     const size_t kstep = (size_t)(BK * 2);
;     const size_t hstep = (size_t)HALF * Kr * 2;
;     const size_t tstep = 2 * hstep;
;     const unsigned ldsw = (unsigned)wid * 1024u;
;     const int aoff = lds_byte(wr * 64 + fr, fq * 8), boff = lds_byte(wc * 32 + fr, fq * 8);
;     ...
;     f32x4 acc[2][2][4][2];
; #pragma unroll
;     for (int a = 0; a < 2; ++a)
; #pragma unroll
;         for (int b = 0; b < 2; ++b)
; #pragma unroll
;             for (int m = 0; m < 4; ++m)
; #pragma unroll
;                 for (int n = 0; n < 2; ++n) acc[a][b][m][n] = (f32x4){0.f, 0.f, 0.f, 0.f};
	s_cbranch_scc1 .LBB0_2171
	s_lshr_b32 s23, s23, 26
	s_add_i32 s23, s22, s23
	v_or_b32_e32 v4, s6, v3
	s_ashr_i32 s43, s23, 6
	v_lshlrev_b32_e32 v5, 4, v1
	v_lshlrev_b32_e32 v6, 6, v4
	s_movk_i32 s23, 0x3c0
	v_lshlrev_b32_e32 v4, 2, v4
	v_and_or_b32 v6, v6, s23, v5
	s_lshl_b32 s23, s45, 13
	v_and_b32_e32 v4, 32, v4
	v_bitop3_b32 v6, v6, s23, v4 bitop3:0xde
	v_lshl_or_b32 v4, v3, 6, v5
	v_lshlrev_b32_e32 v5, 2, v3
	s_lshl_b32 s23, s7, 12
	v_and_b32_e32 v5, 32, v5
	v_bitop3_b32 v152, v4, s23, v5 bitop3:0xde
	v_add_u32_e32 v4, s5, v149
	s_movk_i32 s23, 0x80
	s_add_i32 s44, s43, -2
	v_add3_u32 v4, v4, v148, s23
	v_mad_u64_u32 v[4:5], s[46:47], s22, v4, v[134:135]
	s_add_u32 s24, s0, s24
	v_add_lshl_u32 v4, v4, v151, 1
	v_mov_b32_e32 v5, v131
	s_addc_u32 s25, s1, s25
	v_lshl_add_u64 v[148:149], s[24:25], 0, v[4:5]
	v_add_u32_e32 v4, s5, v154
	v_add3_u32 v4, v4, v153, s23
	v_mad_u64_u32 v[4:5], s[22:23], s22, v4, v[150:151]
	v_add_lshl_u32 v4, v4, v155, 1
	v_mov_b32_e32 v5, v131
	v_mov_b32_e32 v36, 0
	v_mov_b32_e32 v143, v131
	v_mov_b32_e32 v147, v131
	v_lshl_add_u64 v[150:151], s[24:25], 0, v[4:5]
	s_mov_b32 s24, 0
	s_mov_b64 s[22:23], 0x11000080
	v_add_u32_e32 v134, s2, v6
	v_mov_b32_e32 v37, v36
	v_mov_b32_e32 v38, v36
	v_mov_b32_e32 v39, v36
	v_mov_b32_e32 v40, v36
	v_mov_b32_e32 v41, v36
	v_mov_b32_e32 v42, v36
	v_mov_b32_e32 v43, v36
	v_mov_b32_e32 v52, v36
	v_mov_b32_e32 v53, v36
	v_mov_b32_e32 v54, v36
	v_mov_b32_e32 v55, v36
	v_mov_b32_e32 v56, v36
	v_mov_b32_e32 v57, v36
	v_mov_b32_e32 v58, v36
	v_mov_b32_e32 v59, v36
	v_mov_b32_e32 v12, v36
	v_mov_b32_e32 v13, v36
	v_mov_b32_e32 v14, v36
	v_mov_b32_e32 v15, v36
	v_mov_b32_e32 v16, v36
	v_mov_b32_e32 v17, v36
	v_mov_b32_e32 v18, v36
	v_mov_b32_e32 v19, v36
	v_mov_b32_e32 v28, v36
	v_mov_b32_e32 v29, v36
	v_mov_b32_e32 v30, v36
	v_mov_b32_e32 v31, v36
	v_mov_b32_e32 v32, v36
	v_mov_b32_e32 v33, v36
	v_mov_b32_e32 v34, v36
	v_mov_b32_e32 v35, v36
	v_mov_b32_e32 v44, v36
	v_mov_b32_e32 v45, v36
	v_mov_b32_e32 v46, v36
	v_mov_b32_e32 v47, v36
	v_mov_b32_e32 v48, v36
	v_mov_b32_e32 v49, v36
	v_mov_b32_e32 v50, v36
	v_mov_b32_e32 v51, v36
	v_mov_b32_e32 v60, v36
	v_mov_b32_e32 v61, v36
	v_mov_b32_e32 v62, v36
	v_mov_b32_e32 v63, v36
	v_mov_b32_e32 v64, v36
	v_mov_b32_e32 v65, v36
	v_mov_b32_e32 v66, v36
	v_mov_b32_e32 v67, v36
	v_mov_b32_e32 v68, v36
	v_mov_b32_e32 v69, v36
	v_mov_b32_e32 v70, v36
	v_mov_b32_e32 v71, v36
	v_mov_b32_e32 v72, v36
	v_mov_b32_e32 v73, v36
	v_mov_b32_e32 v74, v36
	v_mov_b32_e32 v75, v36
	v_mov_b32_e32 v84, v36
	v_mov_b32_e32 v85, v36
	v_mov_b32_e32 v86, v36
	v_mov_b32_e32 v87, v36
	v_mov_b32_e32 v88, v36
	v_mov_b32_e32 v89, v36
	v_mov_b32_e32 v90, v36
	v_mov_b32_e32 v91, v36
	v_mov_b32_e32 v100, v36
	v_mov_b32_e32 v101, v36
	v_mov_b32_e32 v102, v36
	v_mov_b32_e32 v103, v36
	v_mov_b32_e32 v104, v36
	v_mov_b32_e32 v105, v36
	v_mov_b32_e32 v106, v36
	v_mov_b32_e32 v107, v36
	v_mov_b32_e32 v116, v36
	v_mov_b32_e32 v117, v36
	v_mov_b32_e32 v118, v36
	v_mov_b32_e32 v119, v36
	v_mov_b32_e32 v120, v36
	v_mov_b32_e32 v121, v36
	v_mov_b32_e32 v122, v36
	v_mov_b32_e32 v123, v36
	v_mov_b32_e32 v76, v36
	v_mov_b32_e32 v77, v36
	v_mov_b32_e32 v78, v36
	v_mov_b32_e32 v79, v36
	v_mov_b32_e32 v80, v36
	v_mov_b32_e32 v81, v36
	v_mov_b32_e32 v82, v36
	v_mov_b32_e32 v83, v36
	v_mov_b32_e32 v92, v36
	v_mov_b32_e32 v93, v36
	v_mov_b32_e32 v94, v36
	v_mov_b32_e32 v95, v36
	v_mov_b32_e32 v96, v36
	v_mov_b32_e32 v97, v36
	v_mov_b32_e32 v98, v36
	v_mov_b32_e32 v99, v36
	v_mov_b32_e32 v108, v36
	v_mov_b32_e32 v109, v36
	v_mov_b32_e32 v110, v36
	v_mov_b32_e32 v111, v36
	v_mov_b32_e32 v112, v36
	v_mov_b32_e32 v113, v36
	v_mov_b32_e32 v114, v36
	v_mov_b32_e32 v115, v36
	v_mov_b32_e32 v124, v36
	v_mov_b32_e32 v125, v36
	v_mov_b32_e32 v126, v36
	v_mov_b32_e32 v127, v36
	v_mov_b32_e32 v138, v36
	v_mov_b32_e32 v139, v36
	v_mov_b32_e32 v140, v36
	v_mov_b32_e32 v141, v36
	v_mov_b32_e32 v24, v36
	v_mov_b32_e32 v25, v36
	v_mov_b32_e32 v26, v36
	v_mov_b32_e32 v27, v36
	v_mov_b32_e32 v20, v36
	v_mov_b32_e32 v21, v36
	v_mov_b32_e32 v22, v36
	v_mov_b32_e32 v23, v36
	v_mov_b32_e32 v8, v36
	v_mov_b32_e32 v9, v36
	v_mov_b32_e32 v10, v36
	v_mov_b32_e32 v11, v36
	v_mov_b32_e32 v4, v36
	v_mov_b32_e32 v5, v36
	v_mov_b32_e32 v6, v36
	v_mov_b32_e32 v7, v36
	.p2alignl 6, 3212836864

; template <int K, class Epi, class Sched, bool ALIGN_EPI>
; __device__ __forceinline__ void gemm_phase(LAS unsigned char* lds, const Gemm g, const Sched& S, const Epi& E) {
;     ...
;     f32x4 acc[2][2][4][2];
; #pragma unroll
;     for (int a = 0; a < 2; ++a)
; #pragma unroll
;         for (int b = 0; b < 2; ++b)
; #pragma unroll
;             for (int m = 0; m < 4; ++m)
; #pragma unroll
;                 for (int n = 0; n < 2; ++n) acc[a][b][m][n] = (f32x4){0.f, 0.f, 0.f, 0.f};
.LBB0_2335:
	v_mov_b32_e32 v7, 0
	s_andn2_b64 vcc, exec, s[42:43]
	v_mov_b32_e32 v6, v7
	v_mov_b32_e32 v5, v7
	v_mov_b32_e32 v4, v7
	v_mov_b32_e32 v11, v7
	v_mov_b32_e32 v10, v7
	v_mov_b32_e32 v9, v7
	v_mov_b32_e32 v8, v7
	v_mov_b32_e32 v23, v7
	v_mov_b32_e32 v22, v7
	v_mov_b32_e32 v21, v7
	v_mov_b32_e32 v20, v7
	v_mov_b32_e32 v27, v7
	v_mov_b32_e32 v26, v7
	v_mov_b32_e32 v25, v7
	v_mov_b32_e32 v24, v7
	s_waitcnt vmcnt(0)
	v_mov_b32_e32 v157, v7
	v_mov_b32_e32 v156, v7
	v_mov_b32_e32 v155, v7
	v_mov_b32_e32 v154, v7
	v_mov_b32_e32 v153, v7
	v_mov_b32_e32 v152, v7
	v_mov_b32_e32 v151, v7
	v_mov_b32_e32 v150, v7
	v_mov_b32_e32 v141, v7
	v_mov_b32_e32 v140, v7
	v_mov_b32_e32 v139, v7
	v_mov_b32_e32 v138, v7
	v_mov_b32_e32 v127, v7
	v_mov_b32_e32 v126, v7
	v_mov_b32_e32 v125, v7
	v_mov_b32_e32 v124, v7
	v_mov_b32_e32 v115, v7
	v_mov_b32_e32 v114, v7
	v_mov_b32_e32 v113, v7
	v_mov_b32_e32 v112, v7
	v_mov_b32_e32 v111, v7
	v_mov_b32_e32 v110, v7
	v_mov_b32_e32 v109, v7
	v_mov_b32_e32 v108, v7
	v_mov_b32_e32 v99, v7
	v_mov_b32_e32 v98, v7
	v_mov_b32_e32 v97, v7
	v_mov_b32_e32 v96, v7
	v_mov_b32_e32 v95, v7
	v_mov_b32_e32 v94, v7
	v_mov_b32_e32 v93, v7
	v_mov_b32_e32 v92, v7
	v_mov_b32_e32 v149, v7
	v_mov_b32_e32 v148, v7
	v_mov_b32_e32 v147, v7
	v_mov_b32_e32 v146, v7
	v_mov_b32_e32 v145, v7
	v_mov_b32_e32 v144, v7
	v_mov_b32_e32 v143, v7
	v_mov_b32_e32 v142, v7
	v_mov_b32_e32 v123, v7
	v_mov_b32_e32 v122, v7
	v_mov_b32_e32 v121, v7
	v_mov_b32_e32 v120, v7
	v_mov_b32_e32 v119, v7
	v_mov_b32_e32 v118, v7
	v_mov_b32_e32 v117, v7
	v_mov_b32_e32 v116, v7
	v_mov_b32_e32 v107, v7
	v_mov_b32_e32 v106, v7
	v_mov_b32_e32 v105, v7
	v_mov_b32_e32 v104, v7
	v_mov_b32_e32 v103, v7
	v_mov_b32_e32 v102, v7
	v_mov_b32_e32 v101, v7
	v_mov_b32_e32 v100, v7
	v_mov_b32_e32 v91, v7
	v_mov_b32_e32 v90, v7
	v_mov_b32_e32 v89, v7
	v_mov_b32_e32 v88, v7
	v_mov_b32_e32 v87, v7
	v_mov_b32_e32 v86, v7
	v_mov_b32_e32 v85, v7
	v_mov_b32_e32 v84, v7
	v_mov_b32_e32 v83, v7
	v_mov_b32_e32 v82, v7
	v_mov_b32_e32 v81, v7
	v_mov_b32_e32 v80, v7
	v_mov_b32_e32 v79, v7
	v_mov_b32_e32 v78, v7
	v_mov_b32_e32 v77, v7
	v_mov_b32_e32 v76, v7
	v_mov_b32_e32 v51, v7
	v_mov_b32_e32 v50, v7
	v_mov_b32_e32 v49, v7
	v_mov_b32_e32 v48, v7
	v_mov_b32_e32 v47, v7
	v_mov_b32_e32 v46, v7
	v_mov_b32_e32 v45, v7
	v_mov_b32_e32 v44, v7
	v_mov_b32_e32 v35, v7
	v_mov_b32_e32 v34, v7
	v_mov_b32_e32 v33, v7
	v_mov_b32_e32 v32, v7
	v_mov_b32_e32 v31, v7
	v_mov_b32_e32 v30, v7
	v_mov_b32_e32 v29, v7
	v_mov_b32_e32 v28, v7
	v_mov_b32_e32 v19, v7
	v_mov_b32_e32 v18, v7
	v_mov_b32_e32 v17, v7
	v_mov_b32_e32 v16, v7
	v_mov_b32_e32 v15, v7
	v_mov_b32_e32 v14, v7
	v_mov_b32_e32 v13, v7
	v_mov_b32_e32 v12, v7
	v_mov_b32_e32 v75, v7
	v_mov_b32_e32 v74, v7
	v_mov_b32_e32 v73, v7
	v_mov_b32_e32 v72, v7
	v_mov_b32_e32 v71, v7
	v_mov_b32_e32 v70, v7
	v_mov_b32_e32 v69, v7
	v_mov_b32_e32 v68, v7
	v_mov_b32_e32 v43, v7
	v_mov_b32_e32 v42, v7
	v_mov_b32_e32 v41, v7
	v_mov_b32_e32 v40, v7
	v_mov_b32_e32 v39, v7
	v_mov_b32_e32 v38, v7
	v_mov_b32_e32 v37, v7
	v_mov_b32_e32 v36, v7
	s_cbranch_vccnz .LBB0_2338
	v_mov_b32_e32 v36, 0
	v_mov_b32_e32 v57, v131
	v_mov_b32_e32 v55, v131
	s_mov_b32 s47, 0
	s_mov_b64 s[76:77], 0x100
	s_mov_b64 s[78:79], s[36:37]
	v_mov_b32_e32 v37, v36
	v_mov_b32_e32 v38, v36
	v_mov_b32_e32 v39, v36
	v_mov_b32_e32 v40, v36
	v_mov_b32_e32 v41, v36
	v_mov_b32_e32 v42, v36
	v_mov_b32_e32 v43, v36
	v_mov_b32_e32 v68, v36
	v_mov_b32_e32 v69, v36
	v_mov_b32_e32 v70, v36
	v_mov_b32_e32 v71, v36
	v_mov_b32_e32 v72, v36
	v_mov_b32_e32 v73, v36
	v_mov_b32_e32 v74, v36
	v_mov_b32_e32 v75, v36
	v_mov_b32_e32 v12, v36
	v_mov_b32_e32 v13, v36
	v_mov_b32_e32 v14, v36
	v_mov_b32_e32 v15, v36
	v_mov_b32_e32 v16, v36
	v_mov_b32_e32 v17, v36
	v_mov_b32_e32 v18, v36
	v_mov_b32_e32 v19, v36
	v_mov_b32_e32 v28, v36
	v_mov_b32_e32 v29, v36
	v_mov_b32_e32 v30, v36
	v_mov_b32_e32 v31, v36
	v_mov_b32_e32 v32, v36
	v_mov_b32_e32 v33, v36
	v_mov_b32_e32 v34, v36
	v_mov_b32_e32 v35, v36
	v_mov_b32_e32 v44, v36
	v_mov_b32_e32 v45, v36
	v_mov_b32_e32 v46, v36
	v_mov_b32_e32 v47, v36
	v_mov_b32_e32 v48, v36
	v_mov_b32_e32 v49, v36
	v_mov_b32_e32 v50, v36
	v_mov_b32_e32 v51, v36
	v_mov_b32_e32 v76, v36
	v_mov_b32_e32 v77, v36
	v_mov_b32_e32 v78, v36
	v_mov_b32_e32 v79, v36
	v_mov_b32_e32 v80, v36
	v_mov_b32_e32 v81, v36
	v_mov_b32_e32 v82, v36
	v_mov_b32_e32 v83, v36
	v_mov_b32_e32 v84, v36
	v_mov_b32_e32 v85, v36
	v_mov_b32_e32 v86, v36
	v_mov_b32_e32 v87, v36
	v_mov_b32_e32 v88, v36
	v_mov_b32_e32 v89, v36
	v_mov_b32_e32 v90, v36
	v_mov_b32_e32 v91, v36
	v_mov_b32_e32 v100, v36
	v_mov_b32_e32 v101, v36
	v_mov_b32_e32 v102, v36
	v_mov_b32_e32 v103, v36
	v_mov_b32_e32 v104, v36
	v_mov_b32_e32 v105, v36
	v_mov_b32_e32 v106, v36
	v_mov_b32_e32 v107, v36
	v_mov_b32_e32 v116, v36
	v_mov_b32_e32 v117, v36
	v_mov_b32_e32 v118, v36
	v_mov_b32_e32 v119, v36
	v_mov_b32_e32 v120, v36
	v_mov_b32_e32 v121, v36
	v_mov_b32_e32 v122, v36
	v_mov_b32_e32 v123, v36
	v_mov_b32_e32 v142, v36
	v_mov_b32_e32 v143, v36
	v_mov_b32_e32 v144, v36
	v_mov_b32_e32 v145, v36
	v_mov_b32_e32 v146, v36
	v_mov_b32_e32 v147, v36
	v_mov_b32_e32 v148, v36
	v_mov_b32_e32 v149, v36
	v_mov_b32_e32 v92, v36
	v_mov_b32_e32 v93, v36
	v_mov_b32_e32 v94, v36
	v_mov_b32_e32 v95, v36
	v_mov_b32_e32 v96, v36
	v_mov_b32_e32 v97, v36
	v_mov_b32_e32 v98, v36
	v_mov_b32_e32 v99, v36
	v_mov_b32_e32 v108, v36
	v_mov_b32_e32 v109, v36
	v_mov_b32_e32 v110, v36
	v_mov_b32_e32 v111, v36
	v_mov_b32_e32 v112, v36
	v_mov_b32_e32 v113, v36
	v_mov_b32_e32 v114, v36
	v_mov_b32_e32 v115, v36
	v_mov_b32_e32 v124, v36
	v_mov_b32_e32 v125, v36
	v_mov_b32_e32 v126, v36
	v_mov_b32_e32 v127, v36
	v_mov_b32_e32 v138, v36
	v_mov_b32_e32 v139, v36
	v_mov_b32_e32 v140, v36
	v_mov_b32_e32 v141, v36
	v_mov_b32_e32 v150, v36
	v_mov_b32_e32 v151, v36
	v_mov_b32_e32 v152, v36
	v_mov_b32_e32 v153, v36
	v_mov_b32_e32 v154, v36
	v_mov_b32_e32 v155, v36
	v_mov_b32_e32 v156, v36
	v_mov_b32_e32 v157, v36
	v_mov_b32_e32 v24, v36
	v_mov_b32_e32 v25, v36
	v_mov_b32_e32 v26, v36
	v_mov_b32_e32 v27, v36
	v_mov_b32_e32 v20, v36
	v_mov_b32_e32 v21, v36
	v_mov_b32_e32 v22, v36
	v_mov_b32_e32 v23, v36
	v_mov_b32_e32 v8, v36
	v_mov_b32_e32 v9, v36
	v_mov_b32_e32 v10, v36
	v_mov_b32_e32 v11, v36
	v_mov_b32_e32 v4, v36
	v_mov_b32_e32 v5, v36
	v_mov_b32_e32 v6, v36
	v_mov_b32_e32 v7, v36
	.p2alignl 6, 3212836864
